# S3: S2 + hand-written adj loader (1KB row segments, 8-tile deep, 8-slot LDS mask ring, med3-based mask conversion)
# speedup vs baseline: 1.0154x; 1.0154x over previous
_Z11attn_kernelPKiPKDv8_DF16_PKDF16_S5_PDF16_Pf:
	s_mul_i32 s3, s2, 27
	s_mul_hi_i32 s26, s3, 0x2aaaaaab
	v_and_b32_e32 v102, 63, v0
	s_lshr_b32 s27, s26, 31
	s_ashr_i32 s28, s26, 3
	s_movk_i32 s4, 0x200
	v_lshrrev_b32_e32 v98, 6, v0
	s_add_i32 s28, s28, s27
	v_cmp_gt_u32_e32 vcc, s4, v0
	s_mul_hi_i32 s29, s3, 0x38e38e39
	v_lshlrev_b32_e32 v122, 4, v102
	s_and_saveexec_b64 s[4:5], vcc
	s_xor_b64 s[12:13], exec, s[4:5]
	s_cbranch_execz .LBB1_65
	s_lshr_b32 s6, s29, 31
	s_ashr_i32 s7, s29, 9
	s_add_i32 s6, s7, s6
	s_mul_i32 s7, s6, 0xffffffd0
	v_bfe_u32 v117, v0, 6, 2
	s_add_i32 s7, s7, s28
	v_lshl_or_b32 v4, s6, 2, v117
	s_lshl_b32 s6, s7, 6
	s_load_dwordx2 s[4:5], s[0:1], 0x8
	s_load_dwordx4 s[8:11], s[0:1], 0x18
	s_load_dwordx2 s[14:15], s[0:1], 0x28
	s_movk_i32 s30, 0xc00
	v_mov_b32_e32 v2, s6
	v_and_b32_e32 v119, 31, v0
	v_mad_i32_i24 v2, v4, s30, v2
	v_or_b32_e32 v2, v2, v119
	s_mul_i32 s6, s28, 48
	v_ashrrev_i32_e32 v3, 31, v2
	s_sub_i32 s6, s3, s6
	s_waitcnt lgkmcnt(0)
	v_lshl_add_u64 v[2:3], v[2:3], 1, s[8:9]
	s_lshl_b32 s6, s6, 2
	global_load_ushort v5, v[2:3], off
	global_load_ushort v6, v[2:3], off offset:64
	s_movk_i32 s31, 0xc0
	v_mov_b32_e32 v2, s6
	s_add_i32 s6, s3, 1
	v_mad_i32_i24 v2, v4, s31, v2
	v_lshrrev_b32_e32 v4, 7, v0
	s_mul_hi_i32 s7, s6, 0x2aaaaaab
	v_and_b32_e32 v121, 2, v4
	s_lshr_b32 s16, s7, 31
	s_lshr_b32 s7, s7, 3
	v_or_b32_e32 v2, v2, v121
	s_add_i32 s7, s7, s16
	v_ashrrev_i32_e32 v3, 31, v2
	s_mul_i32 s7, s7, 48
	v_lshlrev_b64 v[2:3], 11, v[2:3]
	s_sub_i32 s7, s6, s7
	s_mul_hi_i32 s6, s6, 0x38e38e39
	v_lshl_add_u64 v[2:3], s[4:5], 0, v[2:3]
	v_mov_b32_e32 v123, 0
	s_lshr_b32 s16, s6, 31
	s_lshr_b32 s6, s6, 9
	v_lshl_add_u64 v[2:3], v[2:3], 0, v[122:123]
	s_add_i32 s6, s6, s16
	global_load_dwordx4 v[86:89], v[2:3], off
	global_load_dwordx4 v[82:85], v[2:3], off offset:1024
	global_load_dwordx4 v[70:73], v[2:3], off offset:2048
	global_load_dwordx4 v[66:69], v[2:3], off offset:3072
	v_lshl_or_b32 v2, s6, 2, v117
	s_lshl_b32 s6, s7, 2
	v_mov_b32_e32 v3, s6
	v_mad_i32_i24 v2, v2, s31, v3
	v_or_b32_e32 v2, v2, v121
	v_ashrrev_i32_e32 v3, 31, v2
	v_lshlrev_b64 v[2:3], 11, v[2:3]
	v_lshl_add_u64 v[2:3], s[4:5], 0, v[2:3]
	v_lshl_add_u64 v[2:3], v[2:3], 0, v[122:123]
	global_load_dwordx4 v[94:97], v[2:3], off
	global_load_dwordx4 v[90:93], v[2:3], off offset:1024
	global_load_dwordx4 v[78:81], v[2:3], off offset:2048
	global_load_dwordx4 v[74:77], v[2:3], off offset:3072
	v_lshlrev_b32_e32 v3, 2, v102
	v_lshrrev_b32_e32 v1, 5, v102
	v_lshl_add_u64 v[114:115], s[4:5], 0, v[122:123]
	s_movk_i32 s4, 0xff
	v_lshl_or_b32 v127, v117, 14, v3
	v_lshlrev_b32_e32 v3, 8, v117
	v_lshlrev_b32_e32 v7, 2, v119
	s_mov_b32 s16, 0x15000
	v_cmp_lt_u32_e64 s[6:7], s4, v0
	v_or3_b32 v128, v3, v7, s16
	v_lshlrev_b32_e32 v3, 10, v1
	v_and_b32_e32 v0, 0xc0, v0
	v_lshlrev_b32_e32 v2, 1, v117
	v_or3_b32 v124, v3, v0, v119
	v_lshlrev_b32_e32 v0, 3, v121
	v_or3_b32 v0, v2, v0, v1
	v_lshlrev_b32_e32 v8, 6, v117
	v_lshlrev_b32_e32 v129, 5, v0
	v_or_b32_e32 v0, 1, v4
	v_or3_b32 v116, v3, v8, v119
	v_lshlrev_b32_e32 v3, 3, v0
	v_lshlrev_b32_e32 v125, 4, v1
	s_movk_i32 s16, 0x80
	v_or3_b32 v1, v2, v3, v1
	v_lshlrev_b32_e32 v133, 5, v0
	s_mov_b32 s36, 0x5040100
	v_mbcnt_lo_u32_b32 v0, -1, 0
	s_add_i32 s33, s3, 2
	v_cmp_gt_u32_e64 s[4:5], 32, v102
	s_lshl_b32 s34, s2, 1
	s_movk_i32 s35, 0x2000
	v_or_b32_e32 v118, 0x2000, v116
	v_or3_b32 v120, v7, v117, s16
	v_add_u32_e32 v126, v7, v98
	v_lshlrev_b32_e32 v130, 5, v121
	v_mul_u32_u24_e32 v131, 0x90, v119
	v_lshlrev_b32_e32 v132, 5, v1
	s_mov_b32 s42, 0
	s_movk_i32 s37, 0x5000
	s_movk_i32 s38, 0x6000
	s_movk_i32 s39, 0x7000
	s_movk_i32 s40, 0x1000
	s_movk_i32 s41, 0x3000
	v_mbcnt_hi_u32_b32 v134, -1, v0
	v_mov_b32_e32 v1, 0
	s_waitcnt vmcnt(9)
	v_perm_b32 v136, v5, v5, s36
	s_waitcnt vmcnt(8)
	v_perm_b32 v135, v6, v6, s36
	v_mov_b32_e32 v122, 0
	v_mov_b32_e32 v18, v123
	v_mov_b32_e32 v19, v123
	v_mov_b32_e32 v20, v123
	v_mov_b32_e32 v21, v123
	v_mov_b32_e32 v22, v123
	v_mov_b32_e32 v23, v123
	v_mov_b32_e32 v24, v123
	v_mov_b32_e32 v25, v123
	v_mov_b32_e32 v26, v123
	v_mov_b32_e32 v27, v123
	v_mov_b32_e32 v28, v123
	v_mov_b32_e32 v29, v123
	v_mov_b32_e32 v30, v123
	v_mov_b32_e32 v31, v123
	v_mov_b32_e32 v32, v123
	v_mov_b32_e32 v33, v123
	v_mov_b32_e32 v50, v123
	v_mov_b32_e32 v51, v123
	v_mov_b32_e32 v52, v123
	v_mov_b32_e32 v53, v123
	v_mov_b32_e32 v54, v123
	v_mov_b32_e32 v55, v123
	v_mov_b32_e32 v56, v123
	v_mov_b32_e32 v57, v123
	v_mov_b32_e32 v58, v123
	v_mov_b32_e32 v59, v123
	v_mov_b32_e32 v60, v123
	v_mov_b32_e32 v61, v123
	v_mov_b32_e32 v62, v123
	v_mov_b32_e32 v63, v123
	v_mov_b32_e32 v64, v123
	v_mov_b32_e32 v65, v123
	v_mov_b32_e32 v2, v123
	v_mov_b32_e32 v3, v123
	v_mov_b32_e32 v4, v123
	v_mov_b32_e32 v5, v123
	v_mov_b32_e32 v6, v123
	v_mov_b32_e32 v7, v123
	v_mov_b32_e32 v8, v123
	v_mov_b32_e32 v9, v123
	v_mov_b32_e32 v10, v123
	v_mov_b32_e32 v11, v123
	v_mov_b32_e32 v12, v123
	v_mov_b32_e32 v13, v123
	v_mov_b32_e32 v14, v123
	v_mov_b32_e32 v15, v123
	v_mov_b32_e32 v16, v123
	v_mov_b32_e32 v17, v123
	v_mov_b32_e32 v34, v123
	v_mov_b32_e32 v35, v123
	v_mov_b32_e32 v36, v123
	v_mov_b32_e32 v37, v123
	v_mov_b32_e32 v38, v123
	v_mov_b32_e32 v39, v123
	v_mov_b32_e32 v40, v123
	v_mov_b32_e32 v41, v123
	v_mov_b32_e32 v42, v123
	v_mov_b32_e32 v43, v123
	v_mov_b32_e32 v44, v123
	v_mov_b32_e32 v45, v123
	v_mov_b32_e32 v46, v123
	v_mov_b32_e32 v47, v123
	v_mov_b32_e32 v48, v123
	v_mov_b32_e32 v49, v123
	v_add3_u32 v137, v125, v130, v131
	v_lshlrev_b32_e32 v118, 4, v134
	v_readfirstlane_b32 s52, v114
	v_readfirstlane_b32 s53, v115
	v_readfirstlane_b32 s57, v117
	v_readfirstlane_b32 s58, v121
	v_bfe_u32 v138, v134, 4, 1
	v_bfe_u32 v139, v134, 3, 1
	v_cmp_eq_u32_e32 vcc, v138, v139
	v_mov_b32_e32 v155, 0x3c003c00
	s_nop 1
	v_cndmask_b32_e32 v154, 0, v155, vcc
	v_mov_b32_e32 v122, 0
	v_mov_b32_e32 v155, v154
	v_mov_b32_e32 v156, v154
	v_mov_b32_e32 v157, v154
	v_mov_b32_e32 v123, 0
	v_mov_b32_e32 v124, 0
	v_mov_b32_e32 v125, 0
	v_mov_b32_e32 v146, 0
	v_mov_b32_e32 v147, 0
	v_mov_b32_e32 v148, 0
	v_mov_b32_e32 v149, 0
	s_mov_b32 s49, s28
	s_mul_i32 s50, s28, 48
	s_sub_i32 s50, s3, s50
	s_add_i32 s50, s50, -1
	s_mov_b32 s55, 87040
	s_mov_b32 s56, 0
	s_mul_hi_u32 s59, s33, 0x2aaaaaab
	s_lshr_b32 s59, s59, 3
	s_mul_i32 s60, s59, 48
	s_sub_i32 s51, s33, s60
	s_mul_hi_u32 s60, s59, 0x2aaaaaab
	s_lshr_b32 s60, s60, 3
	s_mul_i32 s54, s60, 48
	s_sub_i32 s54, s59, s54
	s_lshl_b32 s60, s60, 2
	s_add_i32 s60, s60, s57
	s_mul_i32 s60, s60, 0xc0
	s_lshl_b32 s59, s51, 2
	s_add_i32 s60, s60, s59
	s_add_i32 s60, s60, s58
	s_lshl_b32 s60, s60, 11
	s_add_u32 s52, s52, s60
	s_addc_u32 s53, s53, 0
	s_barrier
	s_branch .LBB1_4

.Lcb_nw0:
	s_waitcnt lgkmcnt(4)
	v_pk_mul_f16 v114, v142, v136
	v_pk_mul_f16 v115, v143, v136
	v_pk_mul_f16 v166, v144, v136
	v_pk_mul_f16 v167, v145, v136
	v_pk_max_u16 v114, v114, v138
	v_pk_max_u16 v115, v115, v139
	v_pk_max_u16 v166, v166, v140
	v_pk_max_u16 v167, v167, v141
	s_waitcnt lgkmcnt(3)
	v_and_b32_e32 v150, v114, v150
	v_and_b32_e32 v151, v115, v151
	v_and_b32_e32 v152, v166, v152
	v_and_b32_e32 v153, v167, v153
	v_pk_mul_f16 v114, v142, v135
	v_pk_mul_f16 v115, v143, v135
	v_pk_mul_f16 v166, v144, v135
	v_pk_mul_f16 v167, v145, v135
	v_pk_max_u16 v114, v114, v138
	v_pk_max_u16 v115, v115, v139
	v_pk_max_u16 v166, v166, v140
	v_pk_max_u16 v167, v167, v141
	ds_read_b128 v[138:141], v0 offset:18688
	ds_read_b128 v[142:145], v0 offset:18704
	s_waitcnt lgkmcnt(4)
	v_and_b32_e32 v158, v114, v158
	v_and_b32_e32 v159, v115, v159
	v_and_b32_e32 v160, v166, v160
	v_and_b32_e32 v161, v167, v161
	s_waitcnt vmcnt(11)
	v_mfma_f32_32x32x16_f16 v[34:49], v[150:153], v[86:89], v[34:49]
	v_mfma_f32_16x16x32_f16 v[122:125], v[150:153], v[154:157], v[122:125]
	v_mfma_f32_32x32x16_f16 v[50:65], v[158:161], v[86:89], v[50:65]
	v_mfma_f32_16x16x32_f16 v[146:149], v[158:161], v[154:157], v[146:149]
	s_waitcnt vmcnt(10)
	v_mfma_f32_32x32x16_f16 v[2:17], v[150:153], v[82:85], v[2:17]
	s_waitcnt lgkmcnt(0)
	v_pk_mul_f16 v114, v142, v136
	v_pk_mul_f16 v115, v143, v136
	v_pk_mul_f16 v166, v144, v136
	v_pk_mul_f16 v167, v145, v136
	v_mfma_f32_32x32x16_f16 v[18:33], v[158:161], v[82:85], v[18:33]
	v_pk_max_u16 v114, v114, v138
	v_pk_max_u16 v115, v115, v139
	v_pk_max_u16 v166, v166, v140
	v_pk_max_u16 v167, v167, v141
	v_and_b32_e32 v162, v114, v162
	v_and_b32_e32 v163, v115, v163
	v_and_b32_e32 v164, v166, v164
	v_and_b32_e32 v165, v167, v165
	v_pk_mul_f16 v114, v142, v135
	v_pk_mul_f16 v115, v143, v135
	v_pk_mul_f16 v166, v144, v135
	v_pk_mul_f16 v167, v145, v135
	v_pk_max_u16 v114, v114, v138
	v_pk_max_u16 v115, v115, v139
	v_pk_max_u16 v166, v166, v140
	v_pk_max_u16 v167, v167, v141
	v_and_b32_e32 v130, v114, v130
	v_and_b32_e32 v131, v115, v131
	v_and_b32_e32 v132, v166, v132
	v_and_b32_e32 v133, v167, v133
	s_waitcnt vmcnt(9)
	v_mfma_f32_32x32x16_f16 v[34:49], v[162:165], v[70:73], v[34:49]
	v_mfma_f32_16x16x32_f16 v[122:125], v[162:165], v[154:157], v[122:125]
	v_mfma_f32_32x32x16_f16 v[50:65], v[130:133], v[70:73], v[50:65]
	v_mfma_f32_16x16x32_f16 v[146:149], v[130:133], v[154:157], v[146:149]
	s_waitcnt vmcnt(8)
	v_mfma_f32_32x32x16_f16 v[2:17], v[162:165], v[66:69], v[2:17]
	s_add_i32 s55, s55, 0x2400
	s_cmp_eq_u32 s55, 160768
	s_cselect_b32 s55, 87040, s55
	s_xor_b32 s56, s56, 0x400
	v_mfma_f32_32x32x16_f16 v[18:33], v[130:133], v[66:69], v[18:33]
	s_mov_b32 s48, s49
	s_cmp_lg_u32 s50, 47
	s_barrier
	s_cbranch_scc1 .LBB1_18
	v_bfe_u32 v138, v134, 2, 2
	v_bfe_u32 v139, v134, 4, 1
	v_lshlrev_b32_e32 v138, 4, v138
	v_lshl_or_b32 v138, v139, 3, v138
	v_lshlrev_b32_e32 v138, 2, v138
	s_nop 4
	ds_bpermute_b32 v140, v138, v122
	ds_bpermute_b32 v141, v138, v123
	ds_bpermute_b32 v142, v138, v124
	ds_bpermute_b32 v143, v138, v125
	ds_bpermute_b32 v144, v138, v146
	ds_bpermute_b32 v145, v138, v147
	ds_bpermute_b32 v150, v138, v148
	ds_bpermute_b32 v151, v138, v149
	v_and_b32_e32 v139, 3, v134
	v_cmp_eq_u32_e64 s[16:17], 1, v139
	v_cmp_eq_u32_e64 s[18:19], 2, v139
	v_cmp_eq_u32_e64 s[20:21], 3, v139
	v_cmp_gt_u32_e64 s[22:23], 32, v134
	s_waitcnt lgkmcnt(0)
	v_cndmask_b32_e64 v140, v140, v141, s[16:17]
	v_cndmask_b32_e64 v144, v144, v145, s[16:17]
	v_cndmask_b32_e64 v140, v140, v142, s[18:19]
	v_cndmask_b32_e64 v144, v144, v150, s[18:19]
	v_cndmask_b32_e64 v140, v140, v143, s[20:21]
	v_cndmask_b32_e64 v144, v144, v151, s[20:21]
	v_cndmask_b32_e64 v122, 0, v140, s[22:23]
	v_cndmask_b32_e64 v1, 0, v144, s[22:23]
	v_mov_b32_e32 v123, 0
	v_mov_b32_e32 v124, v116
	v_or_b32_e32 v118, 0x2000, v116
	v_lshlrev_b32_e32 v139, 2, v119
	s_movk_i32 s16, 0x80
	v_lshl_add_u32 v138, v121, 1, v117
	v_or3_b32 v120, v139, v117, s16
	v_add_u32_e32 v126, v139, v138
	v_and_b32_e32 v66, 64, v134
	v_xor_b32_e32 v0, 32, v134
	v_add_u32_e32 v66, 64, v66
	v_cmp_lt_i32_e32 vcc, v0, v66
	s_nop 1
	v_cndmask_b32_e32 v0, v134, v0, vcc
	v_lshlrev_b32_e32 v0, 2, v0
	ds_bpermute_b32 v66, v0, v122
	ds_bpermute_b32 v0, v0, v1
	s_waitcnt lgkmcnt(1)
	v_add_f32_e32 v66, v122, v66
	s_and_saveexec_b64 s[16:17], s[6:7]
	s_xor_b64 s[16:17], exec, s[16:17]
	s_cbranch_execz .LBB1_9
	ds_write2st64_b32 v127, v34, v35 offset0:80 offset1:81
	ds_write2st64_b32 v127, v36, v37 offset0:82 offset1:83
	ds_write2st64_b32 v127, v38, v39 offset0:84 offset1:85
	ds_write2st64_b32 v127, v40, v41 offset0:86 offset1:87
	ds_write2st64_b32 v127, v42, v43 offset0:88 offset1:89
	ds_write2st64_b32 v127, v44, v45 offset0:90 offset1:91
	ds_write2st64_b32 v127, v46, v47 offset0:92 offset1:93
	ds_write2st64_b32 v127, v48, v49 offset0:94 offset1:95
	ds_write2st64_b32 v127, v2, v3 offset0:96 offset1:97
	ds_write2st64_b32 v127, v4, v5 offset0:98 offset1:99
	ds_write2st64_b32 v127, v6, v7 offset0:100 offset1:101
	ds_write2st64_b32 v127, v8, v9 offset0:102 offset1:103
	ds_write2st64_b32 v127, v10, v11 offset0:104 offset1:105
	ds_write2st64_b32 v127, v12, v13 offset0:106 offset1:107
	ds_write2st64_b32 v127, v14, v15 offset0:108 offset1:109
	ds_write2st64_b32 v127, v16, v17 offset0:110 offset1:111
	s_and_saveexec_b64 s[18:19], s[4:5]
	ds_write_b32 v128, v66
	s_or_b64 exec, exec, s[18:19]

.Lcb_nw1:
	s_waitcnt lgkmcnt(4)
	v_pk_mul_f16 v114, v142, v136
	v_pk_mul_f16 v115, v143, v136
	v_pk_mul_f16 v166, v144, v136
	v_pk_mul_f16 v167, v145, v136
	v_pk_max_u16 v114, v114, v138
	v_pk_max_u16 v115, v115, v139
	v_pk_max_u16 v166, v166, v140
	v_pk_max_u16 v167, v167, v141
	s_waitcnt lgkmcnt(3)
	v_and_b32_e32 v150, v114, v150
	v_and_b32_e32 v151, v115, v151
	v_and_b32_e32 v152, v166, v152
	v_and_b32_e32 v153, v167, v153
	v_pk_mul_f16 v114, v142, v135
	v_pk_mul_f16 v115, v143, v135
	v_pk_mul_f16 v166, v144, v135
	v_pk_mul_f16 v167, v145, v135
	v_pk_max_u16 v114, v114, v138
	v_pk_max_u16 v115, v115, v139
	v_pk_max_u16 v166, v166, v140
	v_pk_max_u16 v167, v167, v141
	ds_read_b128 v[138:141], v0 offset:18688
	ds_read_b128 v[142:145], v0 offset:18704
	s_waitcnt lgkmcnt(4)
	v_and_b32_e32 v158, v114, v158
	v_and_b32_e32 v159, v115, v159
	v_and_b32_e32 v160, v166, v160
	v_and_b32_e32 v161, v167, v161
	s_waitcnt vmcnt(11)
	v_mfma_f32_32x32x16_f16 v[34:49], v[150:153], v[94:97], v[34:49]
	v_mfma_f32_16x16x32_f16 v[122:125], v[150:153], v[154:157], v[122:125]
	v_mfma_f32_32x32x16_f16 v[50:65], v[158:161], v[94:97], v[50:65]
	v_mfma_f32_16x16x32_f16 v[146:149], v[158:161], v[154:157], v[146:149]
	s_waitcnt vmcnt(10)
	v_mfma_f32_32x32x16_f16 v[2:17], v[150:153], v[90:93], v[2:17]
	s_waitcnt lgkmcnt(0)
	v_pk_mul_f16 v114, v142, v136
	v_pk_mul_f16 v115, v143, v136
	v_pk_mul_f16 v166, v144, v136
	v_pk_mul_f16 v167, v145, v136
	v_mfma_f32_32x32x16_f16 v[18:33], v[158:161], v[90:93], v[18:33]
	v_pk_max_u16 v114, v114, v138
	v_pk_max_u16 v115, v115, v139
	v_pk_max_u16 v166, v166, v140
	v_pk_max_u16 v167, v167, v141
	v_and_b32_e32 v162, v114, v162
	v_and_b32_e32 v163, v115, v163
	v_and_b32_e32 v164, v166, v164
	v_and_b32_e32 v165, v167, v165
	v_pk_mul_f16 v114, v142, v135
	v_pk_mul_f16 v115, v143, v135
	v_pk_mul_f16 v166, v144, v135
	v_pk_mul_f16 v167, v145, v135
	v_pk_max_u16 v114, v114, v138
	v_pk_max_u16 v115, v115, v139
	v_pk_max_u16 v166, v166, v140
	v_pk_max_u16 v167, v167, v141
	v_and_b32_e32 v130, v114, v130
	v_and_b32_e32 v131, v115, v131
	v_and_b32_e32 v132, v166, v132
	v_and_b32_e32 v133, v167, v133
	s_waitcnt vmcnt(9)
	v_mfma_f32_32x32x16_f16 v[34:49], v[162:165], v[78:81], v[34:49]
	v_mfma_f32_16x16x32_f16 v[122:125], v[162:165], v[154:157], v[122:125]
	v_mfma_f32_32x32x16_f16 v[50:65], v[130:133], v[78:81], v[50:65]
	v_mfma_f32_16x16x32_f16 v[146:149], v[130:133], v[154:157], v[146:149]
	s_waitcnt vmcnt(8)
	v_mfma_f32_32x32x16_f16 v[2:17], v[162:165], v[74:77], v[2:17]
	s_add_i32 s55, s55, 0x2400
	s_cmp_eq_u32 s55, 160768
	s_cselect_b32 s55, 87040, s55
	s_xor_b32 s56, s56, 0x400
	v_mfma_f32_32x32x16_f16 v[18:33], v[130:133], v[74:77], v[18:33]
	s_mov_b32 s47, s49
	s_cmp_lg_u32 s50, 47
	s_barrier
	s_cbranch_scc1 .LBB1_32
	v_bfe_u32 v138, v134, 2, 2
	v_bfe_u32 v139, v134, 4, 1
	v_lshlrev_b32_e32 v138, 4, v138
	v_lshl_or_b32 v138, v139, 3, v138
	v_lshlrev_b32_e32 v138, 2, v138
	s_nop 4
	ds_bpermute_b32 v140, v138, v122
	ds_bpermute_b32 v141, v138, v123
	ds_bpermute_b32 v142, v138, v124
	ds_bpermute_b32 v143, v138, v125
	ds_bpermute_b32 v144, v138, v146
	ds_bpermute_b32 v145, v138, v147
	ds_bpermute_b32 v150, v138, v148
	ds_bpermute_b32 v151, v138, v149
	v_and_b32_e32 v139, 3, v134
	v_cmp_eq_u32_e64 s[16:17], 1, v139
	v_cmp_eq_u32_e64 s[18:19], 2, v139
	v_cmp_eq_u32_e64 s[20:21], 3, v139
	v_cmp_gt_u32_e64 s[22:23], 32, v134
	s_waitcnt lgkmcnt(0)
	v_cndmask_b32_e64 v140, v140, v141, s[16:17]
	v_cndmask_b32_e64 v144, v144, v145, s[16:17]
	v_cndmask_b32_e64 v140, v140, v142, s[18:19]
	v_cndmask_b32_e64 v144, v144, v150, s[18:19]
	v_cndmask_b32_e64 v140, v140, v143, s[20:21]
	v_cndmask_b32_e64 v144, v144, v151, s[20:21]
	v_cndmask_b32_e64 v122, 0, v140, s[22:23]
	v_cndmask_b32_e64 v1, 0, v144, s[22:23]
	v_mov_b32_e32 v123, 0
	v_mov_b32_e32 v124, v116
	v_or_b32_e32 v118, 0x2000, v116
	v_lshlrev_b32_e32 v139, 2, v119
	s_movk_i32 s16, 0x80
	v_lshl_add_u32 v138, v121, 1, v117
	v_or3_b32 v120, v139, v117, s16
	v_add_u32_e32 v126, v139, v138
	v_and_b32_e32 v74, 64, v134
	v_xor_b32_e32 v0, 32, v134
	v_add_u32_e32 v74, 64, v74
	v_cmp_lt_i32_e32 vcc, v0, v74
	s_nop 1
	v_cndmask_b32_e32 v0, v134, v0, vcc
	v_lshlrev_b32_e32 v0, 2, v0
	ds_bpermute_b32 v74, v0, v122
	ds_bpermute_b32 v0, v0, v1
	s_waitcnt lgkmcnt(1)
	v_add_f32_e32 v74, v122, v74
	s_and_saveexec_b64 s[16:17], s[6:7]
	s_xor_b64 s[16:17], exec, s[16:17]
	s_cbranch_execz .LBB1_23
	ds_write2st64_b32 v127, v34, v35 offset0:80 offset1:81
	ds_write2st64_b32 v127, v36, v37 offset0:82 offset1:83
	ds_write2st64_b32 v127, v38, v39 offset0:84 offset1:85
	ds_write2st64_b32 v127, v40, v41 offset0:86 offset1:87
	ds_write2st64_b32 v127, v42, v43 offset0:88 offset1:89
	ds_write2st64_b32 v127, v44, v45 offset0:90 offset1:91
	ds_write2st64_b32 v127, v46, v47 offset0:92 offset1:93
	ds_write2st64_b32 v127, v48, v49 offset0:94 offset1:95
	ds_write2st64_b32 v127, v2, v3 offset0:96 offset1:97
	ds_write2st64_b32 v127, v4, v5 offset0:98 offset1:99
	ds_write2st64_b32 v127, v6, v7 offset0:100 offset1:101
	ds_write2st64_b32 v127, v8, v9 offset0:102 offset1:103
	ds_write2st64_b32 v127, v10, v11 offset0:104 offset1:105
	ds_write2st64_b32 v127, v12, v13 offset0:106 offset1:107
	ds_write2st64_b32 v127, v14, v15 offset0:108 offset1:109
	ds_write2st64_b32 v127, v16, v17 offset0:110 offset1:111
	s_and_saveexec_b64 s[18:19], s[4:5]
	ds_write_b32 v128, v74
	s_or_b64 exec, exec, s[18:19]

.Lcb_nw2:
	s_waitcnt lgkmcnt(4)
	v_pk_mul_f16 v114, v142, v136
	v_pk_mul_f16 v115, v143, v136
	v_pk_mul_f16 v166, v144, v136
	v_pk_mul_f16 v167, v145, v136
	v_pk_max_u16 v114, v114, v138
	v_pk_max_u16 v115, v115, v139
	v_pk_max_u16 v166, v166, v140
	v_pk_max_u16 v167, v167, v141
	s_waitcnt lgkmcnt(3)
	v_and_b32_e32 v150, v114, v150
	v_and_b32_e32 v151, v115, v151
	v_and_b32_e32 v152, v166, v152
	v_and_b32_e32 v153, v167, v153
	v_pk_mul_f16 v114, v142, v135
	v_pk_mul_f16 v115, v143, v135
	v_pk_mul_f16 v166, v144, v135
	v_pk_mul_f16 v167, v145, v135
	v_pk_max_u16 v114, v114, v138
	v_pk_max_u16 v115, v115, v139
	v_pk_max_u16 v166, v166, v140
	v_pk_max_u16 v167, v167, v141
	ds_read_b128 v[138:141], v0 offset:18688
	ds_read_b128 v[142:145], v0 offset:18704
	s_waitcnt lgkmcnt(4)
	v_and_b32_e32 v158, v114, v158
	v_and_b32_e32 v159, v115, v159
	v_and_b32_e32 v160, v166, v160
	v_and_b32_e32 v161, v167, v161
	s_waitcnt vmcnt(11)
	v_mfma_f32_32x32x16_f16 v[34:49], v[150:153], v[110:113], v[34:49]
	v_mfma_f32_16x16x32_f16 v[122:125], v[150:153], v[154:157], v[122:125]
	v_mfma_f32_32x32x16_f16 v[50:65], v[158:161], v[110:113], v[50:65]
	v_mfma_f32_16x16x32_f16 v[146:149], v[158:161], v[154:157], v[146:149]
	s_waitcnt vmcnt(10)
	v_mfma_f32_32x32x16_f16 v[2:17], v[150:153], v[106:109], v[2:17]
	s_waitcnt lgkmcnt(0)
	v_pk_mul_f16 v114, v142, v136
	v_pk_mul_f16 v115, v143, v136
	v_pk_mul_f16 v166, v144, v136
	v_pk_mul_f16 v167, v145, v136
	v_mfma_f32_32x32x16_f16 v[18:33], v[158:161], v[106:109], v[18:33]
	v_pk_max_u16 v114, v114, v138
	v_pk_max_u16 v115, v115, v139
	v_pk_max_u16 v166, v166, v140
	v_pk_max_u16 v167, v167, v141
	v_and_b32_e32 v162, v114, v162
	v_and_b32_e32 v163, v115, v163
	v_and_b32_e32 v164, v166, v164
	v_and_b32_e32 v165, v167, v165
	v_pk_mul_f16 v114, v142, v135
	v_pk_mul_f16 v115, v143, v135
	v_pk_mul_f16 v166, v144, v135
	v_pk_mul_f16 v167, v145, v135
	v_pk_max_u16 v114, v114, v138
	v_pk_max_u16 v115, v115, v139
	v_pk_max_u16 v166, v166, v140
	v_pk_max_u16 v167, v167, v141
	v_and_b32_e32 v130, v114, v130
	v_and_b32_e32 v131, v115, v131
	v_and_b32_e32 v132, v166, v132
	v_and_b32_e32 v133, v167, v133
	s_waitcnt vmcnt(9)
	v_mfma_f32_32x32x16_f16 v[34:49], v[162:165], v[102:105], v[34:49]
	v_mfma_f32_16x16x32_f16 v[122:125], v[162:165], v[154:157], v[122:125]
	v_mfma_f32_32x32x16_f16 v[50:65], v[130:133], v[102:105], v[50:65]
	v_mfma_f32_16x16x32_f16 v[146:149], v[130:133], v[154:157], v[146:149]
	s_waitcnt vmcnt(8)
	v_mfma_f32_32x32x16_f16 v[2:17], v[162:165], v[98:101], v[2:17]
	s_add_i32 s55, s55, 0x2400
	s_cmp_eq_u32 s55, 160768
	s_cselect_b32 s55, 87040, s55
	s_xor_b32 s56, s56, 0x400
	v_mfma_f32_32x32x16_f16 v[18:33], v[130:133], v[98:101], v[18:33]
	s_mov_b32 s44, s49
	s_cmp_eq_u32 s50, 47
	s_cselect_b32 s16, 1, 0
	s_cmp_eq_u32 s42, 24
	s_cselect_b32 s17, 1, 0
	s_or_b32 s16, s16, s17
	s_barrier
	s_cbranch_scc0 .LBB1_3
	v_bfe_u32 v138, v134, 2, 2
	v_bfe_u32 v139, v134, 4, 1
	v_lshlrev_b32_e32 v138, 4, v138
	v_lshl_or_b32 v138, v139, 3, v138
	v_lshlrev_b32_e32 v138, 2, v138
	s_nop 4
	ds_bpermute_b32 v140, v138, v122
	ds_bpermute_b32 v141, v138, v123
	ds_bpermute_b32 v142, v138, v124
	ds_bpermute_b32 v143, v138, v125
	ds_bpermute_b32 v144, v138, v146
	ds_bpermute_b32 v145, v138, v147
	ds_bpermute_b32 v150, v138, v148
	ds_bpermute_b32 v151, v138, v149
	v_and_b32_e32 v139, 3, v134
	v_cmp_eq_u32_e64 s[16:17], 1, v139
	v_cmp_eq_u32_e64 s[18:19], 2, v139
	v_cmp_eq_u32_e64 s[20:21], 3, v139
	v_cmp_gt_u32_e64 s[22:23], 32, v134
	s_waitcnt lgkmcnt(0)
	v_cndmask_b32_e64 v140, v140, v141, s[16:17]
	v_cndmask_b32_e64 v144, v144, v145, s[16:17]
	v_cndmask_b32_e64 v140, v140, v142, s[18:19]
	v_cndmask_b32_e64 v144, v144, v150, s[18:19]
	v_cndmask_b32_e64 v140, v140, v143, s[20:21]
	v_cndmask_b32_e64 v144, v144, v151, s[20:21]
	v_cndmask_b32_e64 v122, 0, v140, s[22:23]
	v_cndmask_b32_e64 v1, 0, v144, s[22:23]
	v_mov_b32_e32 v123, 0
	v_mov_b32_e32 v124, v116
	v_or_b32_e32 v118, 0x2000, v116
	v_lshlrev_b32_e32 v139, 2, v119
	s_movk_i32 s16, 0x80
	v_lshl_add_u32 v138, v121, 1, v117
	v_or3_b32 v120, v139, v117, s16
	v_add_u32_e32 v126, v139, v138
	v_and_b32_e32 v98, 64, v134
	v_xor_b32_e32 v0, 32, v134
	v_add_u32_e32 v98, 64, v98
	v_cmp_lt_i32_e32 vcc, v0, v98
	s_nop 1
	v_cndmask_b32_e32 v0, v134, v0, vcc
	v_lshlrev_b32_e32 v0, 2, v0
	ds_bpermute_b32 v98, v0, v122
	ds_bpermute_b32 v0, v0, v1
	s_waitcnt lgkmcnt(1)
	v_add_f32_e32 v98, v122, v98
	s_and_saveexec_b64 s[16:17], s[6:7]
	s_xor_b64 s[16:17], exec, s[16:17]
	s_cbranch_execz .LBB1_37
	ds_write2st64_b32 v127, v34, v35 offset0:80 offset1:81
	ds_write2st64_b32 v127, v36, v37 offset0:82 offset1:83
	ds_write2st64_b32 v127, v38, v39 offset0:84 offset1:85
	ds_write2st64_b32 v127, v40, v41 offset0:86 offset1:87
	ds_write2st64_b32 v127, v42, v43 offset0:88 offset1:89
	ds_write2st64_b32 v127, v44, v45 offset0:90 offset1:91
	ds_write2st64_b32 v127, v46, v47 offset0:92 offset1:93
	ds_write2st64_b32 v127, v48, v49 offset0:94 offset1:95
	ds_write2st64_b32 v127, v2, v3 offset0:96 offset1:97
	ds_write2st64_b32 v127, v4, v5 offset0:98 offset1:99
	ds_write2st64_b32 v127, v6, v7 offset0:100 offset1:101
	ds_write2st64_b32 v127, v8, v9 offset0:102 offset1:103
	ds_write2st64_b32 v127, v10, v11 offset0:104 offset1:105
	ds_write2st64_b32 v127, v12, v13 offset0:106 offset1:107
	ds_write2st64_b32 v127, v14, v15 offset0:108 offset1:109
	ds_write2st64_b32 v127, v16, v17 offset0:110 offset1:111
	s_and_saveexec_b64 s[18:19], s[4:5]
	ds_write_b32 v128, v98
	s_or_b64 exec, exec, s[18:19]

.LBB1_65:
	s_andn2_saveexec_b64 s[4:5], s[12:13]
	s_cbranch_execz .LBB1_103
	s_load_dwordx2 s[4:5], s[0:1], 0x0
	s_load_dwordx2 s[6:7], s[0:1], 0x10
	v_mov_b32_e32 v128, v102
	v_readfirstlane_b32 s8, v98
	v_and_b32_e32 v129, 15, v128
	v_lshrrev_b32_e32 v130, 4, v128
	v_lshlrev_b32_e32 v138, 4, v128
	s_add_i32 s8, s8, -8
	s_add_i32 s10, s3, 26
	s_mov_b32 s12, 0x2aaaaaab
	s_mul_i32 s9, s28, 48
	s_sub_i32 s9, s3, s9
	v_lshrrev_b32_e32 v133, 2, v129
	v_and_b32_e32 v134, 1, v129
	v_bfe_u32 v135, v129, 1, 1
	v_lshl_or_b32 v134, v134, 1, v135
	v_lshlrev_b32_e32 v134, 3, v134
	v_lshl_or_b32 v134, v133, 5, v134
	s_mul_i32 s11, s8, 2304
	s_add_i32 s11, s11, 87040
	s_movk_i32 s13, 9216
	v_mad_u32_u24 v131, v130, s13, v134
	v_add_u32_e32 v131, s11, v131
	v_lshlrev_b32_e32 v129, 4, v129
	s_mul_hi_u32 s11, s28, s12
	s_lshr_b32 s11, s11, 3
	s_mul_i32 s17, s11, 48
	s_sub_i32 s17, s28, s17
	s_mov_b32 s16, s9
	s_mul_i32 s11, s11, 192
	s_lshl_b32 s13, s9, 2
	s_add_i32 s11, s11, s13
	s_lshl_b32 s11, s11, 8
	s_waitcnt lgkmcnt(0)
	s_add_u32 s14, s6, s11
	s_addc_u32 s15, s7, 0
	s_mul_i32 s11, s8, 0x30000
	s_add_u32 s64, s4, s11
	s_addc_u32 s65, s5, 0
	s_add_u32 s66, s64, 0x3000
	s_addc_u32 s67, s65, 0
	s_add_u32 s68, s66, 0x3000
	s_addc_u32 s69, s67, 0
	s_add_u32 s70, s68, 0x3000
	s_addc_u32 s71, s69, 0
	s_add_u32 s72, s70, 0x3000
	s_addc_u32 s73, s71, 0
	s_add_u32 s74, s72, 0x3000
	s_addc_u32 s75, s73, 0
	s_add_u32 s76, s74, 0x3000
	s_addc_u32 s77, s75, 0
	s_add_u32 s78, s76, 0x3000
	s_addc_u32 s79, s77, 0
	s_add_u32 s80, s78, 0x3000
	s_addc_u32 s81, s79, 0
	s_add_u32 s82, s80, 0x3000
	s_addc_u32 s83, s81, 0
	s_add_u32 s84, s82, 0x3000
	s_addc_u32 s85, s83, 0
	s_add_u32 s86, s84, 0x3000
	s_addc_u32 s87, s85, 0
	s_add_u32 s88, s86, 0x3000
	s_addc_u32 s89, s87, 0
	s_add_u32 s90, s88, 0x3000
	s_addc_u32 s91, s89, 0
	s_add_u32 s92, s90, 0x3000
	s_addc_u32 s93, s91, 0
	s_add_u32 s94, s92, 0x3000
	s_addc_u32 s95, s93, 0
	global_load_dwordx4 v[140:143], v138, s[14:15]
	s_add_u32 s14, s14, 0x400
	s_addc_u32 s15, s15, 0
	s_add_i32 s16, s16, 1
	s_cmp_lg_u32 s16, 48
	s_cbranch_scc1 .Lld_bbn0
	s_mov_b32 s16, 0
	s_add_i32 s17, s17, 1
	s_cmp_lg_u32 s17, 48
	s_cbranch_scc1 .Lld_bbw0
	s_mov_b32 s17, 0
	s_branch .Lld_bbn0
.Lld_bbw0:
	s_sub_u32 s14, s14, 0xc000
	s_subb_u32 s15, s15, 0
.Lld_bbn0:
	s_add_i32 s11, s3, 0
	v_add_u32_e32 v132, s11, v130
	v_min_u32_e32 v132, s10, v132
	v_mul_hi_u32 v133, v132, s12
	v_lshrrev_b32_e32 v133, 3, v133
	v_mul_u32_u24_e32 v134, 48, v133
	v_sub_u32_e32 v134, v132, v134
	v_mul_u32_u24_e32 v133, 0xc0000, v133
	v_lshl_add_u32 v133, v134, 8, v133
	v_add_u32_e32 v132, v133, v129
	global_load_dwordx4 v[0:3], v132, s[64:65] nt
	global_load_dwordx4 v[4:7], v132, s[66:67] nt
	global_load_dwordx4 v[8:11], v132, s[68:69] nt
	global_load_dwordx4 v[12:15], v132, s[70:71] nt
	global_load_dwordx4 v[16:19], v132, s[72:73] nt
	global_load_dwordx4 v[20:23], v132, s[74:75] nt
	global_load_dwordx4 v[24:27], v132, s[76:77] nt
	global_load_dwordx4 v[28:31], v132, s[78:79] nt
	global_load_dwordx4 v[32:35], v132, s[80:81] nt
	global_load_dwordx4 v[36:39], v132, s[82:83] nt
	global_load_dwordx4 v[40:43], v132, s[84:85] nt
	global_load_dwordx4 v[44:47], v132, s[86:87] nt
	global_load_dwordx4 v[48:51], v132, s[88:89] nt
	global_load_dwordx4 v[52:55], v132, s[90:91] nt
	global_load_dwordx4 v[56:59], v132, s[92:93] nt
	global_load_dwordx4 v[60:63], v132, s[94:95] nt
	global_load_dwordx4 v[144:147], v138, s[14:15]
	s_add_u32 s14, s14, 0x400
	s_addc_u32 s15, s15, 0
	s_add_i32 s16, s16, 1
	s_cmp_lg_u32 s16, 48
	s_cbranch_scc1 .Lld_bbn1
	s_mov_b32 s16, 0
	s_add_i32 s17, s17, 1
	s_cmp_lg_u32 s17, 48
	s_cbranch_scc1 .Lld_bbw1
	s_mov_b32 s17, 0
	s_branch .Lld_bbn1

.Lld_bbn1:
	global_load_dwordx4 v[148:151], v138, s[14:15]
	s_add_u32 s14, s14, 0x400
	s_addc_u32 s15, s15, 0
	s_add_i32 s16, s16, 1
	s_cmp_lg_u32 s16, 48
	s_cbranch_scc1 .Lld_bbn2
	s_mov_b32 s16, 0
	s_add_i32 s17, s17, 1
	s_cmp_lg_u32 s17, 48
	s_cbranch_scc1 .Lld_bbw2
	s_mov_b32 s17, 0
	s_branch .Lld_bbn2

.Lld_bbn2:
	global_load_dwordx4 v[152:155], v138, s[14:15]
	s_add_u32 s14, s14, 0x400
	s_addc_u32 s15, s15, 0
	s_add_i32 s16, s16, 1
	s_cmp_lg_u32 s16, 48
	s_cbranch_scc1 .Lld_bbn3
	s_mov_b32 s16, 0
	s_add_i32 s17, s17, 1
	s_cmp_lg_u32 s17, 48
	s_cbranch_scc1 .Lld_bbw3
	s_mov_b32 s17, 0
	s_branch .Lld_bbn3

.Lld_bbn3:
	global_load_dwordx4 v[156:159], v138, s[14:15]
	s_add_u32 s14, s14, 0x400
	s_addc_u32 s15, s15, 0
	s_add_i32 s16, s16, 1
	s_cmp_lg_u32 s16, 48
	s_cbranch_scc1 .Lld_bbn4
	s_mov_b32 s16, 0
	s_add_i32 s17, s17, 1
	s_cmp_lg_u32 s17, 48
	s_cbranch_scc1 .Lld_bbw4
	s_mov_b32 s17, 0
	s_branch .Lld_bbn4

.Lld_bbn4:
	s_add_i32 s11, s3, 4
	v_add_u32_e32 v132, s11, v130
	v_min_u32_e32 v132, s10, v132
	v_mul_hi_u32 v133, v132, s12
	v_lshrrev_b32_e32 v133, 3, v133
	v_mul_u32_u24_e32 v134, 48, v133
	v_sub_u32_e32 v134, v132, v134
	v_mul_u32_u24_e32 v133, 0xc0000, v133
	v_lshl_add_u32 v133, v134, 8, v133
	v_add_u32_e32 v132, v133, v129
	global_load_dwordx4 v[64:67], v132, s[64:65] nt
	global_load_dwordx4 v[68:71], v132, s[66:67] nt
	global_load_dwordx4 v[72:75], v132, s[68:69] nt
	global_load_dwordx4 v[76:79], v132, s[70:71] nt
	global_load_dwordx4 v[80:83], v132, s[72:73] nt
	global_load_dwordx4 v[84:87], v132, s[74:75] nt
	global_load_dwordx4 v[88:91], v132, s[76:77] nt
	global_load_dwordx4 v[92:95], v132, s[78:79] nt
	global_load_dwordx4 v[96:99], v132, s[80:81] nt
	global_load_dwordx4 v[100:103], v132, s[82:83] nt
	global_load_dwordx4 v[104:107], v132, s[84:85] nt
	global_load_dwordx4 v[108:111], v132, s[86:87] nt
	global_load_dwordx4 v[112:115], v132, s[88:89] nt
	global_load_dwordx4 v[116:119], v132, s[90:91] nt
	global_load_dwordx4 v[120:123], v132, s[92:93] nt
	global_load_dwordx4 v[124:127], v132, s[94:95] nt
	s_waitcnt vmcnt(35)
	v_med3_i32 v0, v0, 0, 1
	v_med3_i32 v1, v1, 0, 1
	v_med3_i32 v2, v2, 0, 1
	v_med3_i32 v3, v3, 0, 1
	v_lshl_or_b32 v0, v1, 16, v0
	v_lshl_or_b32 v1, v3, 16, v2
	v_mul_u32_u24_e32 v0, 0xffff, v0
	v_mul_u32_u24_e32 v1, 0xffff, v1
	ds_write_b64 v131, v[0:1] offset:0
	s_waitcnt vmcnt(34)
	v_med3_i32 v4, v4, 0, 1
	v_med3_i32 v5, v5, 0, 1
	v_med3_i32 v6, v6, 0, 1
	v_med3_i32 v7, v7, 0, 1
	v_lshl_or_b32 v4, v5, 16, v4
	v_lshl_or_b32 v5, v7, 16, v6
	v_mul_u32_u24_e32 v4, 0xffff, v4
	v_mul_u32_u24_e32 v5, 0xffff, v5
	ds_write_b64 v131, v[4:5] offset:144
	s_waitcnt vmcnt(33)
	v_med3_i32 v8, v8, 0, 1
	v_med3_i32 v9, v9, 0, 1
	v_med3_i32 v10, v10, 0, 1
	v_med3_i32 v11, v11, 0, 1
	v_lshl_or_b32 v8, v9, 16, v8
	v_lshl_or_b32 v9, v11, 16, v10
	v_mul_u32_u24_e32 v8, 0xffff, v8
	v_mul_u32_u24_e32 v9, 0xffff, v9
	ds_write_b64 v131, v[8:9] offset:288
	s_waitcnt vmcnt(32)
	v_med3_i32 v12, v12, 0, 1
	v_med3_i32 v13, v13, 0, 1
	v_med3_i32 v14, v14, 0, 1
	v_med3_i32 v15, v15, 0, 1
	v_lshl_or_b32 v12, v13, 16, v12
	v_lshl_or_b32 v13, v15, 16, v14
	v_mul_u32_u24_e32 v12, 0xffff, v12
	v_mul_u32_u24_e32 v13, 0xffff, v13
	ds_write_b64 v131, v[12:13] offset:432
	s_waitcnt vmcnt(31)
	v_med3_i32 v16, v16, 0, 1
	v_med3_i32 v17, v17, 0, 1
	v_med3_i32 v18, v18, 0, 1
	v_med3_i32 v19, v19, 0, 1
	v_lshl_or_b32 v16, v17, 16, v16
	v_lshl_or_b32 v17, v19, 16, v18
	v_mul_u32_u24_e32 v16, 0xffff, v16
	v_mul_u32_u24_e32 v17, 0xffff, v17
	ds_write_b64 v131, v[16:17] offset:576
	s_waitcnt vmcnt(30)
	v_med3_i32 v20, v20, 0, 1
	v_med3_i32 v21, v21, 0, 1
	v_med3_i32 v22, v22, 0, 1
	v_med3_i32 v23, v23, 0, 1
	v_lshl_or_b32 v20, v21, 16, v20
	v_lshl_or_b32 v21, v23, 16, v22
	v_mul_u32_u24_e32 v20, 0xffff, v20
	v_mul_u32_u24_e32 v21, 0xffff, v21
	ds_write_b64 v131, v[20:21] offset:720
	s_waitcnt vmcnt(29)
	v_med3_i32 v24, v24, 0, 1
	v_med3_i32 v25, v25, 0, 1
	v_med3_i32 v26, v26, 0, 1
	v_med3_i32 v27, v27, 0, 1
	v_lshl_or_b32 v24, v25, 16, v24
	v_lshl_or_b32 v25, v27, 16, v26
	v_mul_u32_u24_e32 v24, 0xffff, v24
	v_mul_u32_u24_e32 v25, 0xffff, v25
	ds_write_b64 v131, v[24:25] offset:864
	s_waitcnt vmcnt(28)
	v_med3_i32 v28, v28, 0, 1
	v_med3_i32 v29, v29, 0, 1
	v_med3_i32 v30, v30, 0, 1
	v_med3_i32 v31, v31, 0, 1
	v_lshl_or_b32 v28, v29, 16, v28
	v_lshl_or_b32 v29, v31, 16, v30
	v_mul_u32_u24_e32 v28, 0xffff, v28
	v_mul_u32_u24_e32 v29, 0xffff, v29
	ds_write_b64 v131, v[28:29] offset:1008
	s_waitcnt vmcnt(27)
	v_med3_i32 v32, v32, 0, 1
	v_med3_i32 v33, v33, 0, 1
	v_med3_i32 v34, v34, 0, 1
	v_med3_i32 v35, v35, 0, 1
	v_lshl_or_b32 v32, v33, 16, v32
	v_lshl_or_b32 v33, v35, 16, v34
	v_mul_u32_u24_e32 v32, 0xffff, v32
	v_mul_u32_u24_e32 v33, 0xffff, v33
	ds_write_b64 v131, v[32:33] offset:1152
	s_waitcnt vmcnt(26)
	v_med3_i32 v36, v36, 0, 1
	v_med3_i32 v37, v37, 0, 1
	v_med3_i32 v38, v38, 0, 1
	v_med3_i32 v39, v39, 0, 1
	v_lshl_or_b32 v36, v37, 16, v36
	v_lshl_or_b32 v37, v39, 16, v38
	v_mul_u32_u24_e32 v36, 0xffff, v36
	v_mul_u32_u24_e32 v37, 0xffff, v37
	ds_write_b64 v131, v[36:37] offset:1296
	s_waitcnt vmcnt(25)
	v_med3_i32 v40, v40, 0, 1
	v_med3_i32 v41, v41, 0, 1
	v_med3_i32 v42, v42, 0, 1
	v_med3_i32 v43, v43, 0, 1
	v_lshl_or_b32 v40, v41, 16, v40
	v_lshl_or_b32 v41, v43, 16, v42
	v_mul_u32_u24_e32 v40, 0xffff, v40
	v_mul_u32_u24_e32 v41, 0xffff, v41
	ds_write_b64 v131, v[40:41] offset:1440
	s_waitcnt vmcnt(24)
	v_med3_i32 v44, v44, 0, 1
	v_med3_i32 v45, v45, 0, 1
	v_med3_i32 v46, v46, 0, 1
	v_med3_i32 v47, v47, 0, 1
	v_lshl_or_b32 v44, v45, 16, v44
	v_lshl_or_b32 v45, v47, 16, v46
	v_mul_u32_u24_e32 v44, 0xffff, v44
	v_mul_u32_u24_e32 v45, 0xffff, v45
	ds_write_b64 v131, v[44:45] offset:1584
	s_waitcnt vmcnt(23)
	v_med3_i32 v48, v48, 0, 1
	v_med3_i32 v49, v49, 0, 1
	v_med3_i32 v50, v50, 0, 1
	v_med3_i32 v51, v51, 0, 1
	v_lshl_or_b32 v48, v49, 16, v48
	v_lshl_or_b32 v49, v51, 16, v50
	v_mul_u32_u24_e32 v48, 0xffff, v48
	v_mul_u32_u24_e32 v49, 0xffff, v49
	ds_write_b64 v131, v[48:49] offset:1728
	s_waitcnt vmcnt(22)
	v_med3_i32 v52, v52, 0, 1
	v_med3_i32 v53, v53, 0, 1
	v_med3_i32 v54, v54, 0, 1
	v_med3_i32 v55, v55, 0, 1
	v_lshl_or_b32 v52, v53, 16, v52
	v_lshl_or_b32 v53, v55, 16, v54
	v_mul_u32_u24_e32 v52, 0xffff, v52
	v_mul_u32_u24_e32 v53, 0xffff, v53
	ds_write_b64 v131, v[52:53] offset:1872
	s_waitcnt vmcnt(21)
	v_med3_i32 v56, v56, 0, 1
	v_med3_i32 v57, v57, 0, 1
	v_med3_i32 v58, v58, 0, 1
	v_med3_i32 v59, v59, 0, 1
	v_lshl_or_b32 v56, v57, 16, v56
	v_lshl_or_b32 v57, v59, 16, v58
	v_mul_u32_u24_e32 v56, 0xffff, v56
	v_mul_u32_u24_e32 v57, 0xffff, v57
	ds_write_b64 v131, v[56:57] offset:2016
	s_waitcnt vmcnt(20)
	v_med3_i32 v60, v60, 0, 1
	v_med3_i32 v61, v61, 0, 1
	v_med3_i32 v62, v62, 0, 1
	v_med3_i32 v63, v63, 0, 1
	v_lshl_or_b32 v60, v61, 16, v60
	v_lshl_or_b32 v61, v63, 16, v62
	v_mul_u32_u24_e32 v60, 0xffff, v60
	v_mul_u32_u24_e32 v61, 0xffff, v61
	ds_write_b64 v131, v[60:61] offset:2160
	s_waitcnt vmcnt(36)
	s_cmp_lg_u32 s8, 0
	s_cbranch_scc1 .Lld_bbs0
	ds_write_b128 v138, v[140:143] offset:18432
.Lld_bbs0:
	s_waitcnt lgkmcnt(0)
	s_add_i32 s11, s3, 8
	v_add_u32_e32 v132, s11, v130
	v_min_u32_e32 v132, s10, v132
	v_mul_hi_u32 v133, v132, s12
	v_lshrrev_b32_e32 v133, 3, v133
	v_mul_u32_u24_e32 v134, 48, v133
	v_sub_u32_e32 v134, v132, v134
	v_mul_u32_u24_e32 v133, 0xc0000, v133
	v_lshl_add_u32 v133, v134, 8, v133
	v_add_u32_e32 v132, v133, v129
	global_load_dwordx4 v[0:3], v132, s[64:65] nt
	global_load_dwordx4 v[4:7], v132, s[66:67] nt
	global_load_dwordx4 v[8:11], v132, s[68:69] nt
	global_load_dwordx4 v[12:15], v132, s[70:71] nt
	global_load_dwordx4 v[16:19], v132, s[72:73] nt
	global_load_dwordx4 v[20:23], v132, s[74:75] nt
	global_load_dwordx4 v[24:27], v132, s[76:77] nt
	global_load_dwordx4 v[28:31], v132, s[78:79] nt
	global_load_dwordx4 v[32:35], v132, s[80:81] nt
	global_load_dwordx4 v[36:39], v132, s[82:83] nt
	global_load_dwordx4 v[40:43], v132, s[84:85] nt
	global_load_dwordx4 v[44:47], v132, s[86:87] nt
	global_load_dwordx4 v[48:51], v132, s[88:89] nt
	global_load_dwordx4 v[52:55], v132, s[90:91] nt
	global_load_dwordx4 v[56:59], v132, s[92:93] nt
	global_load_dwordx4 v[60:63], v132, s[94:95] nt
	s_barrier
	s_waitcnt vmcnt(31)
	v_med3_i32 v64, v64, 0, 1
	v_med3_i32 v65, v65, 0, 1
	v_med3_i32 v66, v66, 0, 1
	v_med3_i32 v67, v67, 0, 1
	v_lshl_or_b32 v64, v65, 16, v64
	v_lshl_or_b32 v65, v67, 16, v66
	v_mul_u32_u24_e32 v64, 0xffff, v64
	v_mul_u32_u24_e32 v65, 0xffff, v65
	ds_write_b64 v131, v[64:65] offset:36864
	s_waitcnt vmcnt(30)
	v_med3_i32 v68, v68, 0, 1
	v_med3_i32 v69, v69, 0, 1
	v_med3_i32 v70, v70, 0, 1
	v_med3_i32 v71, v71, 0, 1
	v_lshl_or_b32 v68, v69, 16, v68
	v_lshl_or_b32 v69, v71, 16, v70
	v_mul_u32_u24_e32 v68, 0xffff, v68
	v_mul_u32_u24_e32 v69, 0xffff, v69
	ds_write_b64 v131, v[68:69] offset:37008
	s_waitcnt vmcnt(29)
	v_med3_i32 v72, v72, 0, 1
	v_med3_i32 v73, v73, 0, 1
	v_med3_i32 v74, v74, 0, 1
	v_med3_i32 v75, v75, 0, 1
	v_lshl_or_b32 v72, v73, 16, v72
	v_lshl_or_b32 v73, v75, 16, v74
	v_mul_u32_u24_e32 v72, 0xffff, v72
	v_mul_u32_u24_e32 v73, 0xffff, v73
	ds_write_b64 v131, v[72:73] offset:37152
	s_waitcnt vmcnt(28)
	v_med3_i32 v76, v76, 0, 1
	v_med3_i32 v77, v77, 0, 1
	v_med3_i32 v78, v78, 0, 1
	v_med3_i32 v79, v79, 0, 1
	v_lshl_or_b32 v76, v77, 16, v76
	v_lshl_or_b32 v77, v79, 16, v78
	v_mul_u32_u24_e32 v76, 0xffff, v76
	v_mul_u32_u24_e32 v77, 0xffff, v77
	ds_write_b64 v131, v[76:77] offset:37296
	s_waitcnt vmcnt(35)
	s_cmp_lg_u32 s8, 0
	s_cbranch_scc1 .Lld_bbs1
	ds_write_b128 v138, v[144:147] offset:19456
.Lld_bbs1:
	s_waitcnt lgkmcnt(0)
	s_add_i32 s11, s3, 12
	v_add_u32_e32 v132, s11, v130
	v_min_u32_e32 v132, s10, v132
	v_mul_hi_u32 v133, v132, s12
	v_lshrrev_b32_e32 v133, 3, v133
	v_mul_u32_u24_e32 v134, 48, v133
	v_sub_u32_e32 v134, v132, v134
	v_mul_u32_u24_e32 v133, 0xc0000, v133
	v_lshl_add_u32 v133, v134, 8, v133
	v_add_u32_e32 v132, v133, v129
	global_load_dwordx4 v[64:67], v132, s[64:65] nt
	global_load_dwordx4 v[68:71], v132, s[66:67] nt
	global_load_dwordx4 v[72:75], v132, s[68:69] nt
	global_load_dwordx4 v[76:79], v132, s[70:71] nt
	global_load_dwordx4 v[140:143], v138, s[14:15]
	s_add_u32 s14, s14, 0x400
	s_addc_u32 s15, s15, 0
	s_add_i32 s16, s16, 1
	s_cmp_lg_u32 s16, 48
	s_cbranch_scc1 .Lld_bbn5
	s_mov_b32 s16, 0
	s_add_i32 s17, s17, 1
	s_cmp_lg_u32 s17, 48
	s_cbranch_scc1 .Lld_bbw5
	s_mov_b32 s17, 0
	s_branch .Lld_bbn5

.Lld_bbn5:
	s_barrier
	s_cmp_lg_u32 s9, 47
	s_cbranch_scc1 .Lld_nf0
	s_barrier
.Lld_nf0:
	s_add_i32 s9, s9, 1
	s_cmp_eq_u32 s9, 48
	s_cselect_b32 s9, 0, s9
	s_waitcnt vmcnt(32)
	v_med3_i32 v80, v80, 0, 1
	v_med3_i32 v81, v81, 0, 1
	v_med3_i32 v82, v82, 0, 1
	v_med3_i32 v83, v83, 0, 1
	v_lshl_or_b32 v80, v81, 16, v80
	v_lshl_or_b32 v81, v83, 16, v82
	v_mul_u32_u24_e32 v80, 0xffff, v80
	v_mul_u32_u24_e32 v81, 0xffff, v81
	ds_write_b64 v131, v[80:81] offset:37440
	s_waitcnt vmcnt(31)
	v_med3_i32 v84, v84, 0, 1
	v_med3_i32 v85, v85, 0, 1
	v_med3_i32 v86, v86, 0, 1
	v_med3_i32 v87, v87, 0, 1
	v_lshl_or_b32 v84, v85, 16, v84
	v_lshl_or_b32 v85, v87, 16, v86
	v_mul_u32_u24_e32 v84, 0xffff, v84
	v_mul_u32_u24_e32 v85, 0xffff, v85
	ds_write_b64 v131, v[84:85] offset:37584
	s_waitcnt vmcnt(30)
	v_med3_i32 v88, v88, 0, 1
	v_med3_i32 v89, v89, 0, 1
	v_med3_i32 v90, v90, 0, 1
	v_med3_i32 v91, v91, 0, 1
	v_lshl_or_b32 v88, v89, 16, v88
	v_lshl_or_b32 v89, v91, 16, v90
	v_mul_u32_u24_e32 v88, 0xffff, v88
	v_mul_u32_u24_e32 v89, 0xffff, v89
	ds_write_b64 v131, v[88:89] offset:37728
	s_waitcnt vmcnt(29)
	v_med3_i32 v92, v92, 0, 1
	v_med3_i32 v93, v93, 0, 1
	v_med3_i32 v94, v94, 0, 1
	v_med3_i32 v95, v95, 0, 1
	v_lshl_or_b32 v92, v93, 16, v92
	v_lshl_or_b32 v93, v95, 16, v94
	v_mul_u32_u24_e32 v92, 0xffff, v92
	v_mul_u32_u24_e32 v93, 0xffff, v93
	ds_write_b64 v131, v[92:93] offset:37872
	s_waitcnt vmcnt(39)
	s_cmp_lg_u32 s8, 0
	s_cbranch_scc1 .Lld_bbs2
	ds_write_b128 v138, v[148:151] offset:18432
.Lld_bbs2:
	s_waitcnt lgkmcnt(0)
	global_load_dwordx4 v[80:83], v132, s[72:73] nt
	global_load_dwordx4 v[84:87], v132, s[74:75] nt
	global_load_dwordx4 v[88:91], v132, s[76:77] nt
	global_load_dwordx4 v[92:95], v132, s[78:79] nt
	global_load_dwordx4 v[144:147], v138, s[14:15]
	s_add_u32 s14, s14, 0x400
	s_addc_u32 s15, s15, 0
	s_add_i32 s16, s16, 1
	s_cmp_lg_u32 s16, 48
	s_cbranch_scc1 .Lld_bbn6
	s_mov_b32 s16, 0
	s_add_i32 s17, s17, 1
	s_cmp_lg_u32 s17, 48
	s_cbranch_scc1 .Lld_bbw6
	s_mov_b32 s17, 0
	s_branch .Lld_bbn6

.Lld_nf1:
	s_add_i32 s9, s9, 1
	s_cmp_eq_u32 s9, 48
	s_cselect_b32 s9, 0, s9
	s_waitcnt vmcnt(33)
	v_med3_i32 v96, v96, 0, 1
	v_med3_i32 v97, v97, 0, 1
	v_med3_i32 v98, v98, 0, 1
	v_med3_i32 v99, v99, 0, 1
	v_lshl_or_b32 v96, v97, 16, v96
	v_lshl_or_b32 v97, v99, 16, v98
	v_mul_u32_u24_e32 v96, 0xffff, v96
	v_mul_u32_u24_e32 v97, 0xffff, v97
	ds_write_b64 v131, v[96:97] offset:38016
	s_waitcnt vmcnt(32)
	v_med3_i32 v100, v100, 0, 1
	v_med3_i32 v101, v101, 0, 1
	v_med3_i32 v102, v102, 0, 1
	v_med3_i32 v103, v103, 0, 1
	v_lshl_or_b32 v100, v101, 16, v100
	v_lshl_or_b32 v101, v103, 16, v102
	v_mul_u32_u24_e32 v100, 0xffff, v100
	v_mul_u32_u24_e32 v101, 0xffff, v101
	ds_write_b64 v131, v[100:101] offset:38160
	s_waitcnt vmcnt(31)
	v_med3_i32 v104, v104, 0, 1
	v_med3_i32 v105, v105, 0, 1
	v_med3_i32 v106, v106, 0, 1
	v_med3_i32 v107, v107, 0, 1
	v_lshl_or_b32 v104, v105, 16, v104
	v_lshl_or_b32 v105, v107, 16, v106
	v_mul_u32_u24_e32 v104, 0xffff, v104
	v_mul_u32_u24_e32 v105, 0xffff, v105
	ds_write_b64 v131, v[104:105] offset:38304
	s_waitcnt vmcnt(30)
	v_med3_i32 v108, v108, 0, 1
	v_med3_i32 v109, v109, 0, 1
	v_med3_i32 v110, v110, 0, 1
	v_med3_i32 v111, v111, 0, 1
	v_lshl_or_b32 v108, v109, 16, v108
	v_lshl_or_b32 v109, v111, 16, v110
	v_mul_u32_u24_e32 v108, 0xffff, v108
	v_mul_u32_u24_e32 v109, 0xffff, v109
	ds_write_b64 v131, v[108:109] offset:38448
	s_waitcnt vmcnt(43)
	s_cmp_lg_u32 s8, 0
	s_cbranch_scc1 .Lld_bbs3
	ds_write_b128 v138, v[152:155] offset:19456
.Lld_bbs3:
	s_waitcnt lgkmcnt(0)
	global_load_dwordx4 v[96:99], v132, s[80:81] nt
	global_load_dwordx4 v[100:103], v132, s[82:83] nt
	global_load_dwordx4 v[104:107], v132, s[84:85] nt
	global_load_dwordx4 v[108:111], v132, s[86:87] nt
	global_load_dwordx4 v[148:151], v138, s[14:15]
	s_add_u32 s14, s14, 0x400
	s_addc_u32 s15, s15, 0
	s_add_i32 s16, s16, 1
	s_cmp_lg_u32 s16, 48
	s_cbranch_scc1 .Lld_bbn7
	s_mov_b32 s16, 0
	s_add_i32 s17, s17, 1
	s_cmp_lg_u32 s17, 48
	s_cbranch_scc1 .Lld_bbw7
	s_mov_b32 s17, 0
	s_branch .Lld_bbn7

.Lld_nf2:
	s_add_i32 s9, s9, 1
	s_cmp_eq_u32 s9, 48
	s_cselect_b32 s9, 0, s9
	s_waitcnt vmcnt(34)
	v_med3_i32 v112, v112, 0, 1
	v_med3_i32 v113, v113, 0, 1
	v_med3_i32 v114, v114, 0, 1
	v_med3_i32 v115, v115, 0, 1
	v_lshl_or_b32 v112, v113, 16, v112
	v_lshl_or_b32 v113, v115, 16, v114
	v_mul_u32_u24_e32 v112, 0xffff, v112
	v_mul_u32_u24_e32 v113, 0xffff, v113
	ds_write_b64 v131, v[112:113] offset:38592
	s_waitcnt vmcnt(33)
	v_med3_i32 v116, v116, 0, 1
	v_med3_i32 v117, v117, 0, 1
	v_med3_i32 v118, v118, 0, 1
	v_med3_i32 v119, v119, 0, 1
	v_lshl_or_b32 v116, v117, 16, v116
	v_lshl_or_b32 v117, v119, 16, v118
	v_mul_u32_u24_e32 v116, 0xffff, v116
	v_mul_u32_u24_e32 v117, 0xffff, v117
	ds_write_b64 v131, v[116:117] offset:38736
	s_waitcnt vmcnt(32)
	v_med3_i32 v120, v120, 0, 1
	v_med3_i32 v121, v121, 0, 1
	v_med3_i32 v122, v122, 0, 1
	v_med3_i32 v123, v123, 0, 1
	v_lshl_or_b32 v120, v121, 16, v120
	v_lshl_or_b32 v121, v123, 16, v122
	v_mul_u32_u24_e32 v120, 0xffff, v120
	v_mul_u32_u24_e32 v121, 0xffff, v121
	ds_write_b64 v131, v[120:121] offset:38880
	s_waitcnt vmcnt(31)
	v_med3_i32 v124, v124, 0, 1
	v_med3_i32 v125, v125, 0, 1
	v_med3_i32 v126, v126, 0, 1
	v_med3_i32 v127, v127, 0, 1
	v_lshl_or_b32 v124, v125, 16, v124
	v_lshl_or_b32 v125, v127, 16, v126
	v_mul_u32_u24_e32 v124, 0xffff, v124
	v_mul_u32_u24_e32 v125, 0xffff, v125
	ds_write_b64 v131, v[124:125] offset:39024
	s_waitcnt vmcnt(47)
	s_cmp_lg_u32 s8, 0
	s_cbranch_scc1 .Lld_bbs4
	ds_write_b128 v138, v[156:159] offset:18432
.Lld_bbs4:
	s_waitcnt lgkmcnt(0)
	global_load_dwordx4 v[112:115], v132, s[88:89] nt
	global_load_dwordx4 v[116:119], v132, s[90:91] nt
	global_load_dwordx4 v[120:123], v132, s[92:93] nt
	global_load_dwordx4 v[124:127], v132, s[94:95] nt
	global_load_dwordx4 v[152:155], v138, s[14:15]
	s_add_u32 s14, s14, 0x400
	s_addc_u32 s15, s15, 0
	s_add_i32 s16, s16, 1
	s_cmp_lg_u32 s16, 48
	s_cbranch_scc1 .Lld_bbn8
	s_mov_b32 s16, 0
	s_add_i32 s17, s17, 1
	s_cmp_lg_u32 s17, 48
	s_cbranch_scc1 .Lld_bbw8
	s_mov_b32 s17, 0
	s_branch .Lld_bbn8

.Lld_nf3:
	s_add_i32 s9, s9, 1
	s_cmp_eq_u32 s9, 48
	s_cselect_b32 s9, 0, s9
	s_waitcnt vmcnt(35)
	v_med3_i32 v0, v0, 0, 1
	v_med3_i32 v1, v1, 0, 1
	v_med3_i32 v2, v2, 0, 1
	v_med3_i32 v3, v3, 0, 1
	v_lshl_or_b32 v0, v1, 16, v0
	v_lshl_or_b32 v1, v3, 16, v2
	v_mul_u32_u24_e32 v0, 0xffff, v0
	v_mul_u32_u24_e32 v1, 0xffff, v1
	ds_write_b64 v131, v[0:1] offset:0
	s_waitcnt vmcnt(34)
	v_med3_i32 v4, v4, 0, 1
	v_med3_i32 v5, v5, 0, 1
	v_med3_i32 v6, v6, 0, 1
	v_med3_i32 v7, v7, 0, 1
	v_lshl_or_b32 v4, v5, 16, v4
	v_lshl_or_b32 v5, v7, 16, v6
	v_mul_u32_u24_e32 v4, 0xffff, v4
	v_mul_u32_u24_e32 v5, 0xffff, v5
	ds_write_b64 v131, v[4:5] offset:144
	s_waitcnt vmcnt(33)
	v_med3_i32 v8, v8, 0, 1
	v_med3_i32 v9, v9, 0, 1
	v_med3_i32 v10, v10, 0, 1
	v_med3_i32 v11, v11, 0, 1
	v_lshl_or_b32 v8, v9, 16, v8
	v_lshl_or_b32 v9, v11, 16, v10
	v_mul_u32_u24_e32 v8, 0xffff, v8
	v_mul_u32_u24_e32 v9, 0xffff, v9
	ds_write_b64 v131, v[8:9] offset:288
	s_waitcnt vmcnt(32)
	v_med3_i32 v12, v12, 0, 1
	v_med3_i32 v13, v13, 0, 1
	v_med3_i32 v14, v14, 0, 1
	v_med3_i32 v15, v15, 0, 1
	v_lshl_or_b32 v12, v13, 16, v12
	v_lshl_or_b32 v13, v15, 16, v14
	v_mul_u32_u24_e32 v12, 0xffff, v12
	v_mul_u32_u24_e32 v13, 0xffff, v13
	ds_write_b64 v131, v[12:13] offset:432
	s_waitcnt vmcnt(15)
	s_cmp_lg_u32 s8, 0
	s_cbranch_scc1 .Lld_bbs5
	ds_write_b128 v138, v[140:143] offset:19456
.Lld_bbs5:
	s_waitcnt lgkmcnt(0)
	s_add_i32 s11, s3, 16
	v_add_u32_e32 v132, s11, v130
	v_min_u32_e32 v132, s10, v132
	v_mul_hi_u32 v133, v132, s12
	v_lshrrev_b32_e32 v133, 3, v133
	v_mul_u32_u24_e32 v134, 48, v133
	v_sub_u32_e32 v134, v132, v134
	v_mul_u32_u24_e32 v133, 0xc0000, v133
	v_lshl_add_u32 v133, v134, 8, v133
	v_add_u32_e32 v132, v133, v129
	global_load_dwordx4 v[0:3], v132, s[64:65] nt
	global_load_dwordx4 v[4:7], v132, s[66:67] nt
	global_load_dwordx4 v[8:11], v132, s[68:69] nt
	global_load_dwordx4 v[12:15], v132, s[70:71] nt
	global_load_dwordx4 v[156:159], v138, s[14:15]
	s_add_u32 s14, s14, 0x400
	s_addc_u32 s15, s15, 0
	s_add_i32 s16, s16, 1
	s_cmp_lg_u32 s16, 48
	s_cbranch_scc1 .Lld_bbn9
	s_mov_b32 s16, 0
	s_add_i32 s17, s17, 1
	s_cmp_lg_u32 s17, 48
	s_cbranch_scc1 .Lld_bbw9
	s_mov_b32 s17, 0
	s_branch .Lld_bbn9

.Lld_nf4:
	s_add_i32 s9, s9, 1
	s_cmp_eq_u32 s9, 48
	s_cselect_b32 s9, 0, s9
	s_waitcnt vmcnt(36)
	v_med3_i32 v16, v16, 0, 1
	v_med3_i32 v17, v17, 0, 1
	v_med3_i32 v18, v18, 0, 1
	v_med3_i32 v19, v19, 0, 1
	v_lshl_or_b32 v16, v17, 16, v16
	v_lshl_or_b32 v17, v19, 16, v18
	v_mul_u32_u24_e32 v16, 0xffff, v16
	v_mul_u32_u24_e32 v17, 0xffff, v17
	ds_write_b64 v131, v[16:17] offset:576
	s_waitcnt vmcnt(35)
	v_med3_i32 v20, v20, 0, 1
	v_med3_i32 v21, v21, 0, 1
	v_med3_i32 v22, v22, 0, 1
	v_med3_i32 v23, v23, 0, 1
	v_lshl_or_b32 v20, v21, 16, v20
	v_lshl_or_b32 v21, v23, 16, v22
	v_mul_u32_u24_e32 v20, 0xffff, v20
	v_mul_u32_u24_e32 v21, 0xffff, v21
	ds_write_b64 v131, v[20:21] offset:720
	s_waitcnt vmcnt(34)
	v_med3_i32 v24, v24, 0, 1
	v_med3_i32 v25, v25, 0, 1
	v_med3_i32 v26, v26, 0, 1
	v_med3_i32 v27, v27, 0, 1
	v_lshl_or_b32 v24, v25, 16, v24
	v_lshl_or_b32 v25, v27, 16, v26
	v_mul_u32_u24_e32 v24, 0xffff, v24
	v_mul_u32_u24_e32 v25, 0xffff, v25
	ds_write_b64 v131, v[24:25] offset:864
	s_waitcnt vmcnt(33)
	v_med3_i32 v28, v28, 0, 1
	v_med3_i32 v29, v29, 0, 1
	v_med3_i32 v30, v30, 0, 1
	v_med3_i32 v31, v31, 0, 1
	v_lshl_or_b32 v28, v29, 16, v28
	v_lshl_or_b32 v29, v31, 16, v30
	v_mul_u32_u24_e32 v28, 0xffff, v28
	v_mul_u32_u24_e32 v29, 0xffff, v29
	ds_write_b64 v131, v[28:29] offset:1008
	s_waitcnt vmcnt(15)
	s_cmp_lg_u32 s8, 0
	s_cbranch_scc1 .Lld_bbs6
	ds_write_b128 v138, v[144:147] offset:18432
.Lld_bbs6:
	s_waitcnt lgkmcnt(0)
	global_load_dwordx4 v[16:19], v132, s[72:73] nt
	global_load_dwordx4 v[20:23], v132, s[74:75] nt
	global_load_dwordx4 v[24:27], v132, s[76:77] nt
	global_load_dwordx4 v[28:31], v132, s[78:79] nt
	global_load_dwordx4 v[140:143], v138, s[14:15]
	s_add_u32 s14, s14, 0x400
	s_addc_u32 s15, s15, 0
	s_add_i32 s16, s16, 1
	s_cmp_lg_u32 s16, 48
	s_cbranch_scc1 .Lld_bbn10
	s_mov_b32 s16, 0
	s_add_i32 s17, s17, 1
	s_cmp_lg_u32 s17, 48
	s_cbranch_scc1 .Lld_bbw10
	s_mov_b32 s17, 0
	s_branch .Lld_bbn10

.Lld_nf5:
	s_add_i32 s9, s9, 1
	s_cmp_eq_u32 s9, 48
	s_cselect_b32 s9, 0, s9
	s_waitcnt vmcnt(37)
	v_med3_i32 v32, v32, 0, 1
	v_med3_i32 v33, v33, 0, 1
	v_med3_i32 v34, v34, 0, 1
	v_med3_i32 v35, v35, 0, 1
	v_lshl_or_b32 v32, v33, 16, v32
	v_lshl_or_b32 v33, v35, 16, v34
	v_mul_u32_u24_e32 v32, 0xffff, v32
	v_mul_u32_u24_e32 v33, 0xffff, v33
	ds_write_b64 v131, v[32:33] offset:1152
	s_waitcnt vmcnt(36)
	v_med3_i32 v36, v36, 0, 1
	v_med3_i32 v37, v37, 0, 1
	v_med3_i32 v38, v38, 0, 1
	v_med3_i32 v39, v39, 0, 1
	v_lshl_or_b32 v36, v37, 16, v36
	v_lshl_or_b32 v37, v39, 16, v38
	v_mul_u32_u24_e32 v36, 0xffff, v36
	v_mul_u32_u24_e32 v37, 0xffff, v37
	ds_write_b64 v131, v[36:37] offset:1296
	s_waitcnt vmcnt(35)
	v_med3_i32 v40, v40, 0, 1
	v_med3_i32 v41, v41, 0, 1
	v_med3_i32 v42, v42, 0, 1
	v_med3_i32 v43, v43, 0, 1
	v_lshl_or_b32 v40, v41, 16, v40
	v_lshl_or_b32 v41, v43, 16, v42
	v_mul_u32_u24_e32 v40, 0xffff, v40
	v_mul_u32_u24_e32 v41, 0xffff, v41
	ds_write_b64 v131, v[40:41] offset:1440
	s_waitcnt vmcnt(34)
	v_med3_i32 v44, v44, 0, 1
	v_med3_i32 v45, v45, 0, 1
	v_med3_i32 v46, v46, 0, 1
	v_med3_i32 v47, v47, 0, 1
	v_lshl_or_b32 v44, v45, 16, v44
	v_lshl_or_b32 v45, v47, 16, v46
	v_mul_u32_u24_e32 v44, 0xffff, v44
	v_mul_u32_u24_e32 v45, 0xffff, v45
	ds_write_b64 v131, v[44:45] offset:1584
	s_waitcnt vmcnt(15)
	s_cmp_lg_u32 s8, 0
	s_cbranch_scc1 .Lld_bbs7
	ds_write_b128 v138, v[148:151] offset:19456
.Lld_bbs7:
	s_waitcnt lgkmcnt(0)
	global_load_dwordx4 v[32:35], v132, s[80:81] nt
	global_load_dwordx4 v[36:39], v132, s[82:83] nt
	global_load_dwordx4 v[40:43], v132, s[84:85] nt
	global_load_dwordx4 v[44:47], v132, s[86:87] nt
	global_load_dwordx4 v[144:147], v138, s[14:15]
	s_add_u32 s14, s14, 0x400
	s_addc_u32 s15, s15, 0
	s_add_i32 s16, s16, 1
	s_cmp_lg_u32 s16, 48
	s_cbranch_scc1 .Lld_bbn11
	s_mov_b32 s16, 0
	s_add_i32 s17, s17, 1
	s_cmp_lg_u32 s17, 48
	s_cbranch_scc1 .Lld_bbw11
	s_mov_b32 s17, 0
	s_branch .Lld_bbn11

.Lld_nf6:
	s_add_i32 s9, s9, 1
	s_cmp_eq_u32 s9, 48
	s_cselect_b32 s9, 0, s9
	s_waitcnt vmcnt(38)
	v_med3_i32 v48, v48, 0, 1
	v_med3_i32 v49, v49, 0, 1
	v_med3_i32 v50, v50, 0, 1
	v_med3_i32 v51, v51, 0, 1
	v_lshl_or_b32 v48, v49, 16, v48
	v_lshl_or_b32 v49, v51, 16, v50
	v_mul_u32_u24_e32 v48, 0xffff, v48
	v_mul_u32_u24_e32 v49, 0xffff, v49
	ds_write_b64 v131, v[48:49] offset:1728
	s_waitcnt vmcnt(37)
	v_med3_i32 v52, v52, 0, 1
	v_med3_i32 v53, v53, 0, 1
	v_med3_i32 v54, v54, 0, 1
	v_med3_i32 v55, v55, 0, 1
	v_lshl_or_b32 v52, v53, 16, v52
	v_lshl_or_b32 v53, v55, 16, v54
	v_mul_u32_u24_e32 v52, 0xffff, v52
	v_mul_u32_u24_e32 v53, 0xffff, v53
	ds_write_b64 v131, v[52:53] offset:1872
	s_waitcnt vmcnt(36)
	v_med3_i32 v56, v56, 0, 1
	v_med3_i32 v57, v57, 0, 1
	v_med3_i32 v58, v58, 0, 1
	v_med3_i32 v59, v59, 0, 1
	v_lshl_or_b32 v56, v57, 16, v56
	v_lshl_or_b32 v57, v59, 16, v58
	v_mul_u32_u24_e32 v56, 0xffff, v56
	v_mul_u32_u24_e32 v57, 0xffff, v57
	ds_write_b64 v131, v[56:57] offset:2016
	s_waitcnt vmcnt(35)
	v_med3_i32 v60, v60, 0, 1
	v_med3_i32 v61, v61, 0, 1
	v_med3_i32 v62, v62, 0, 1
	v_med3_i32 v63, v63, 0, 1
	v_lshl_or_b32 v60, v61, 16, v60
	v_lshl_or_b32 v61, v63, 16, v62
	v_mul_u32_u24_e32 v60, 0xffff, v60
	v_mul_u32_u24_e32 v61, 0xffff, v61
	ds_write_b64 v131, v[60:61] offset:2160
	s_waitcnt vmcnt(15)
	s_cmp_lg_u32 s8, 0
	s_cbranch_scc1 .Lld_bbs8
	ds_write_b128 v138, v[152:155] offset:18432
.Lld_bbs8:
	s_waitcnt lgkmcnt(0)
	global_load_dwordx4 v[48:51], v132, s[88:89] nt
	global_load_dwordx4 v[52:55], v132, s[90:91] nt
	global_load_dwordx4 v[56:59], v132, s[92:93] nt
	global_load_dwordx4 v[60:63], v132, s[94:95] nt
	global_load_dwordx4 v[148:151], v138, s[14:15]
	s_add_u32 s14, s14, 0x400
	s_addc_u32 s15, s15, 0
	s_add_i32 s16, s16, 1
	s_cmp_lg_u32 s16, 48
	s_cbranch_scc1 .Lld_bbn12
	s_mov_b32 s16, 0
	s_add_i32 s17, s17, 1
	s_cmp_lg_u32 s17, 48
	s_cbranch_scc1 .Lld_bbw12
	s_mov_b32 s17, 0
	s_branch .Lld_bbn12

.Lld_nf7:
	s_add_i32 s9, s9, 1
	s_cmp_eq_u32 s9, 48
	s_cselect_b32 s9, 0, s9
	s_waitcnt vmcnt(39)
	v_med3_i32 v64, v64, 0, 1
	v_med3_i32 v65, v65, 0, 1
	v_med3_i32 v66, v66, 0, 1
	v_med3_i32 v67, v67, 0, 1
	v_lshl_or_b32 v64, v65, 16, v64
	v_lshl_or_b32 v65, v67, 16, v66
	v_mul_u32_u24_e32 v64, 0xffff, v64
	v_mul_u32_u24_e32 v65, 0xffff, v65
	ds_write_b64 v131, v[64:65] offset:36864
	s_waitcnt vmcnt(38)
	v_med3_i32 v68, v68, 0, 1
	v_med3_i32 v69, v69, 0, 1
	v_med3_i32 v70, v70, 0, 1
	v_med3_i32 v71, v71, 0, 1
	v_lshl_or_b32 v68, v69, 16, v68
	v_lshl_or_b32 v69, v71, 16, v70
	v_mul_u32_u24_e32 v68, 0xffff, v68
	v_mul_u32_u24_e32 v69, 0xffff, v69
	ds_write_b64 v131, v[68:69] offset:37008
	s_waitcnt vmcnt(37)
	v_med3_i32 v72, v72, 0, 1
	v_med3_i32 v73, v73, 0, 1
	v_med3_i32 v74, v74, 0, 1
	v_med3_i32 v75, v75, 0, 1
	v_lshl_or_b32 v72, v73, 16, v72
	v_lshl_or_b32 v73, v75, 16, v74
	v_mul_u32_u24_e32 v72, 0xffff, v72
	v_mul_u32_u24_e32 v73, 0xffff, v73
	ds_write_b64 v131, v[72:73] offset:37152
	s_waitcnt vmcnt(36)
	v_med3_i32 v76, v76, 0, 1
	v_med3_i32 v77, v77, 0, 1
	v_med3_i32 v78, v78, 0, 1
	v_med3_i32 v79, v79, 0, 1
	v_lshl_or_b32 v76, v77, 16, v76
	v_lshl_or_b32 v77, v79, 16, v78
	v_mul_u32_u24_e32 v76, 0xffff, v76
	v_mul_u32_u24_e32 v77, 0xffff, v77
	ds_write_b64 v131, v[76:77] offset:37296
	s_waitcnt vmcnt(15)
	s_cmp_lg_u32 s8, 0
	s_cbranch_scc1 .Lld_bbs9
	ds_write_b128 v138, v[156:159] offset:19456
.Lld_bbs9:
	s_waitcnt lgkmcnt(0)
	s_add_i32 s11, s3, 20
	v_add_u32_e32 v132, s11, v130
	v_min_u32_e32 v132, s10, v132
	v_mul_hi_u32 v133, v132, s12
	v_lshrrev_b32_e32 v133, 3, v133
	v_mul_u32_u24_e32 v134, 48, v133
	v_sub_u32_e32 v134, v132, v134
	v_mul_u32_u24_e32 v133, 0xc0000, v133
	v_lshl_add_u32 v133, v134, 8, v133
	v_add_u32_e32 v132, v133, v129
	global_load_dwordx4 v[64:67], v132, s[64:65] nt
	global_load_dwordx4 v[68:71], v132, s[66:67] nt
	global_load_dwordx4 v[72:75], v132, s[68:69] nt
	global_load_dwordx4 v[76:79], v132, s[70:71] nt
	global_load_dwordx4 v[152:155], v138, s[14:15]
	s_add_u32 s14, s14, 0x400
	s_addc_u32 s15, s15, 0
	s_add_i32 s16, s16, 1
	s_cmp_lg_u32 s16, 48
	s_cbranch_scc1 .Lld_bbn13
	s_mov_b32 s16, 0
	s_add_i32 s17, s17, 1
	s_cmp_lg_u32 s17, 48
	s_cbranch_scc1 .Lld_bbw13
	s_mov_b32 s17, 0
	s_branch .Lld_bbn13

.Lld_nf8:
	s_add_i32 s9, s9, 1
	s_cmp_eq_u32 s9, 48
	s_cselect_b32 s9, 0, s9
	s_waitcnt vmcnt(39)
	v_med3_i32 v80, v80, 0, 1
	v_med3_i32 v81, v81, 0, 1
	v_med3_i32 v82, v82, 0, 1
	v_med3_i32 v83, v83, 0, 1
	v_lshl_or_b32 v80, v81, 16, v80
	v_lshl_or_b32 v81, v83, 16, v82
	v_mul_u32_u24_e32 v80, 0xffff, v80
	v_mul_u32_u24_e32 v81, 0xffff, v81
	ds_write_b64 v131, v[80:81] offset:37440
	s_waitcnt vmcnt(38)
	v_med3_i32 v84, v84, 0, 1
	v_med3_i32 v85, v85, 0, 1
	v_med3_i32 v86, v86, 0, 1
	v_med3_i32 v87, v87, 0, 1
	v_lshl_or_b32 v84, v85, 16, v84
	v_lshl_or_b32 v85, v87, 16, v86
	v_mul_u32_u24_e32 v84, 0xffff, v84
	v_mul_u32_u24_e32 v85, 0xffff, v85
	ds_write_b64 v131, v[84:85] offset:37584
	s_waitcnt vmcnt(37)
	v_med3_i32 v88, v88, 0, 1
	v_med3_i32 v89, v89, 0, 1
	v_med3_i32 v90, v90, 0, 1
	v_med3_i32 v91, v91, 0, 1
	v_lshl_or_b32 v88, v89, 16, v88
	v_lshl_or_b32 v89, v91, 16, v90
	v_mul_u32_u24_e32 v88, 0xffff, v88
	v_mul_u32_u24_e32 v89, 0xffff, v89
	ds_write_b64 v131, v[88:89] offset:37728
	s_waitcnt vmcnt(36)
	v_med3_i32 v92, v92, 0, 1
	v_med3_i32 v93, v93, 0, 1
	v_med3_i32 v94, v94, 0, 1
	v_med3_i32 v95, v95, 0, 1
	v_lshl_or_b32 v92, v93, 16, v92
	v_lshl_or_b32 v93, v95, 16, v94
	v_mul_u32_u24_e32 v92, 0xffff, v92
	v_mul_u32_u24_e32 v93, 0xffff, v93
	ds_write_b64 v131, v[92:93] offset:37872
	s_waitcnt vmcnt(15)
	s_cmp_lg_u32 s8, 0
	s_cbranch_scc1 .Lld_bbs10
	ds_write_b128 v138, v[140:143] offset:18432
.Lld_bbs10:
	s_waitcnt lgkmcnt(0)
	global_load_dwordx4 v[80:83], v132, s[72:73] nt
	global_load_dwordx4 v[84:87], v132, s[74:75] nt
	global_load_dwordx4 v[88:91], v132, s[76:77] nt
	global_load_dwordx4 v[92:95], v132, s[78:79] nt
	global_load_dwordx4 v[156:159], v138, s[14:15]
	s_add_u32 s14, s14, 0x400
	s_addc_u32 s15, s15, 0
	s_add_i32 s16, s16, 1
	s_cmp_lg_u32 s16, 48
	s_cbranch_scc1 .Lld_bbn14
	s_mov_b32 s16, 0
	s_add_i32 s17, s17, 1
	s_cmp_lg_u32 s17, 48
	s_cbranch_scc1 .Lld_bbw14
	s_mov_b32 s17, 0
	s_branch .Lld_bbn14

.Lld_nf9:
	s_add_i32 s9, s9, 1
	s_cmp_eq_u32 s9, 48
	s_cselect_b32 s9, 0, s9
	s_waitcnt vmcnt(39)
	v_med3_i32 v96, v96, 0, 1
	v_med3_i32 v97, v97, 0, 1
	v_med3_i32 v98, v98, 0, 1
	v_med3_i32 v99, v99, 0, 1
	v_lshl_or_b32 v96, v97, 16, v96
	v_lshl_or_b32 v97, v99, 16, v98
	v_mul_u32_u24_e32 v96, 0xffff, v96
	v_mul_u32_u24_e32 v97, 0xffff, v97
	ds_write_b64 v131, v[96:97] offset:38016
	s_waitcnt vmcnt(38)
	v_med3_i32 v100, v100, 0, 1
	v_med3_i32 v101, v101, 0, 1
	v_med3_i32 v102, v102, 0, 1
	v_med3_i32 v103, v103, 0, 1
	v_lshl_or_b32 v100, v101, 16, v100
	v_lshl_or_b32 v101, v103, 16, v102
	v_mul_u32_u24_e32 v100, 0xffff, v100
	v_mul_u32_u24_e32 v101, 0xffff, v101
	ds_write_b64 v131, v[100:101] offset:38160
	s_waitcnt vmcnt(37)
	v_med3_i32 v104, v104, 0, 1
	v_med3_i32 v105, v105, 0, 1
	v_med3_i32 v106, v106, 0, 1
	v_med3_i32 v107, v107, 0, 1
	v_lshl_or_b32 v104, v105, 16, v104
	v_lshl_or_b32 v105, v107, 16, v106
	v_mul_u32_u24_e32 v104, 0xffff, v104
	v_mul_u32_u24_e32 v105, 0xffff, v105
	ds_write_b64 v131, v[104:105] offset:38304
	s_waitcnt vmcnt(36)
	v_med3_i32 v108, v108, 0, 1
	v_med3_i32 v109, v109, 0, 1
	v_med3_i32 v110, v110, 0, 1
	v_med3_i32 v111, v111, 0, 1
	v_lshl_or_b32 v108, v109, 16, v108
	v_lshl_or_b32 v109, v111, 16, v110
	v_mul_u32_u24_e32 v108, 0xffff, v108
	v_mul_u32_u24_e32 v109, 0xffff, v109
	ds_write_b64 v131, v[108:109] offset:38448
	s_waitcnt vmcnt(15)
	s_cmp_lg_u32 s8, 0
	s_cbranch_scc1 .Lld_bbs11
	ds_write_b128 v138, v[144:147] offset:19456
.Lld_bbs11:
	s_waitcnt lgkmcnt(0)
	global_load_dwordx4 v[96:99], v132, s[80:81] nt
	global_load_dwordx4 v[100:103], v132, s[82:83] nt
	global_load_dwordx4 v[104:107], v132, s[84:85] nt
	global_load_dwordx4 v[108:111], v132, s[86:87] nt
	global_load_dwordx4 v[140:143], v138, s[14:15]
	s_add_u32 s14, s14, 0x400
	s_addc_u32 s15, s15, 0
	s_add_i32 s16, s16, 1
	s_cmp_lg_u32 s16, 48
	s_cbranch_scc1 .Lld_bbn15
	s_mov_b32 s16, 0
	s_add_i32 s17, s17, 1
	s_cmp_lg_u32 s17, 48
	s_cbranch_scc1 .Lld_bbw15
	s_mov_b32 s17, 0
	s_branch .Lld_bbn15

.Lld_nf10:
	s_add_i32 s9, s9, 1
	s_cmp_eq_u32 s9, 48
	s_cselect_b32 s9, 0, s9
	s_waitcnt vmcnt(39)
	v_med3_i32 v112, v112, 0, 1
	v_med3_i32 v113, v113, 0, 1
	v_med3_i32 v114, v114, 0, 1
	v_med3_i32 v115, v115, 0, 1
	v_lshl_or_b32 v112, v113, 16, v112
	v_lshl_or_b32 v113, v115, 16, v114
	v_mul_u32_u24_e32 v112, 0xffff, v112
	v_mul_u32_u24_e32 v113, 0xffff, v113
	ds_write_b64 v131, v[112:113] offset:38592
	s_waitcnt vmcnt(38)
	v_med3_i32 v116, v116, 0, 1
	v_med3_i32 v117, v117, 0, 1
	v_med3_i32 v118, v118, 0, 1
	v_med3_i32 v119, v119, 0, 1
	v_lshl_or_b32 v116, v117, 16, v116
	v_lshl_or_b32 v117, v119, 16, v118
	v_mul_u32_u24_e32 v116, 0xffff, v116
	v_mul_u32_u24_e32 v117, 0xffff, v117
	ds_write_b64 v131, v[116:117] offset:38736
	s_waitcnt vmcnt(37)
	v_med3_i32 v120, v120, 0, 1
	v_med3_i32 v121, v121, 0, 1
	v_med3_i32 v122, v122, 0, 1
	v_med3_i32 v123, v123, 0, 1
	v_lshl_or_b32 v120, v121, 16, v120
	v_lshl_or_b32 v121, v123, 16, v122
	v_mul_u32_u24_e32 v120, 0xffff, v120
	v_mul_u32_u24_e32 v121, 0xffff, v121
	ds_write_b64 v131, v[120:121] offset:38880
	s_waitcnt vmcnt(36)
	v_med3_i32 v124, v124, 0, 1
	v_med3_i32 v125, v125, 0, 1
	v_med3_i32 v126, v126, 0, 1
	v_med3_i32 v127, v127, 0, 1
	v_lshl_or_b32 v124, v125, 16, v124
	v_lshl_or_b32 v125, v127, 16, v126
	v_mul_u32_u24_e32 v124, 0xffff, v124
	v_mul_u32_u24_e32 v125, 0xffff, v125
	ds_write_b64 v131, v[124:125] offset:39024
	s_waitcnt vmcnt(15)
	s_cmp_lg_u32 s8, 0
	s_cbranch_scc1 .Lld_bbs12
	ds_write_b128 v138, v[148:151] offset:18432
.Lld_bbs12:
	s_waitcnt lgkmcnt(0)
	global_load_dwordx4 v[112:115], v132, s[88:89] nt
	global_load_dwordx4 v[116:119], v132, s[90:91] nt
	global_load_dwordx4 v[120:123], v132, s[92:93] nt
	global_load_dwordx4 v[124:127], v132, s[94:95] nt
	global_load_dwordx4 v[144:147], v138, s[14:15]
	s_add_u32 s14, s14, 0x400
	s_addc_u32 s15, s15, 0
	s_add_i32 s16, s16, 1
	s_cmp_lg_u32 s16, 48
	s_cbranch_scc1 .Lld_bbn16
	s_mov_b32 s16, 0
	s_add_i32 s17, s17, 1
	s_cmp_lg_u32 s17, 48
	s_cbranch_scc1 .Lld_bbw16
	s_mov_b32 s17, 0
	s_branch .Lld_bbn16

.Lld_nf11:
	s_add_i32 s9, s9, 1
	s_cmp_eq_u32 s9, 48
	s_cselect_b32 s9, 0, s9
	s_waitcnt vmcnt(39)
	v_med3_i32 v0, v0, 0, 1
	v_med3_i32 v1, v1, 0, 1
	v_med3_i32 v2, v2, 0, 1
	v_med3_i32 v3, v3, 0, 1
	v_lshl_or_b32 v0, v1, 16, v0
	v_lshl_or_b32 v1, v3, 16, v2
	v_mul_u32_u24_e32 v0, 0xffff, v0
	v_mul_u32_u24_e32 v1, 0xffff, v1
	ds_write_b64 v131, v[0:1] offset:0
	s_waitcnt vmcnt(38)
	v_med3_i32 v4, v4, 0, 1
	v_med3_i32 v5, v5, 0, 1
	v_med3_i32 v6, v6, 0, 1
	v_med3_i32 v7, v7, 0, 1
	v_lshl_or_b32 v4, v5, 16, v4
	v_lshl_or_b32 v5, v7, 16, v6
	v_mul_u32_u24_e32 v4, 0xffff, v4
	v_mul_u32_u24_e32 v5, 0xffff, v5
	ds_write_b64 v131, v[4:5] offset:144
	s_waitcnt vmcnt(37)
	v_med3_i32 v8, v8, 0, 1
	v_med3_i32 v9, v9, 0, 1
	v_med3_i32 v10, v10, 0, 1
	v_med3_i32 v11, v11, 0, 1
	v_lshl_or_b32 v8, v9, 16, v8
	v_lshl_or_b32 v9, v11, 16, v10
	v_mul_u32_u24_e32 v8, 0xffff, v8
	v_mul_u32_u24_e32 v9, 0xffff, v9
	ds_write_b64 v131, v[8:9] offset:288
	s_waitcnt vmcnt(36)
	v_med3_i32 v12, v12, 0, 1
	v_med3_i32 v13, v13, 0, 1
	v_med3_i32 v14, v14, 0, 1
	v_med3_i32 v15, v15, 0, 1
	v_lshl_or_b32 v12, v13, 16, v12
	v_lshl_or_b32 v13, v15, 16, v14
	v_mul_u32_u24_e32 v12, 0xffff, v12
	v_mul_u32_u24_e32 v13, 0xffff, v13
	ds_write_b64 v131, v[12:13] offset:432
	s_waitcnt vmcnt(15)
	s_cmp_lg_u32 s8, 0
	s_cbranch_scc1 .Lld_bbs13
	ds_write_b128 v138, v[152:155] offset:19456
.Lld_bbs13:
	s_waitcnt lgkmcnt(0)
	s_add_i32 s11, s3, 24
	v_add_u32_e32 v132, s11, v130
	v_min_u32_e32 v132, s10, v132
	v_mul_hi_u32 v133, v132, s12
	v_lshrrev_b32_e32 v133, 3, v133
	v_mul_u32_u24_e32 v134, 48, v133
	v_sub_u32_e32 v134, v132, v134
	v_mul_u32_u24_e32 v133, 0xc0000, v133
	v_lshl_add_u32 v133, v134, 8, v133
	v_add_u32_e32 v132, v133, v129
	global_load_dwordx4 v[0:3], v132, s[64:65] nt
	global_load_dwordx4 v[4:7], v132, s[66:67] nt
	global_load_dwordx4 v[8:11], v132, s[68:69] nt
	global_load_dwordx4 v[12:15], v132, s[70:71] nt
	global_load_dwordx4 v[148:151], v138, s[14:15]
	s_add_u32 s14, s14, 0x400
	s_addc_u32 s15, s15, 0
	s_add_i32 s16, s16, 1
	s_cmp_lg_u32 s16, 48
	s_cbranch_scc1 .Lld_bbn17
	s_mov_b32 s16, 0
	s_add_i32 s17, s17, 1
	s_cmp_lg_u32 s17, 48
	s_cbranch_scc1 .Lld_bbw17
	s_mov_b32 s17, 0
	s_branch .Lld_bbn17

.Lld_nf12:
	s_add_i32 s9, s9, 1
	s_cmp_eq_u32 s9, 48
	s_cselect_b32 s9, 0, s9
	s_waitcnt vmcnt(39)
	v_med3_i32 v16, v16, 0, 1
	v_med3_i32 v17, v17, 0, 1
	v_med3_i32 v18, v18, 0, 1
	v_med3_i32 v19, v19, 0, 1
	v_lshl_or_b32 v16, v17, 16, v16
	v_lshl_or_b32 v17, v19, 16, v18
	v_mul_u32_u24_e32 v16, 0xffff, v16
	v_mul_u32_u24_e32 v17, 0xffff, v17
	ds_write_b64 v131, v[16:17] offset:576
	s_waitcnt vmcnt(38)
	v_med3_i32 v20, v20, 0, 1
	v_med3_i32 v21, v21, 0, 1
	v_med3_i32 v22, v22, 0, 1
	v_med3_i32 v23, v23, 0, 1
	v_lshl_or_b32 v20, v21, 16, v20
	v_lshl_or_b32 v21, v23, 16, v22
	v_mul_u32_u24_e32 v20, 0xffff, v20
	v_mul_u32_u24_e32 v21, 0xffff, v21
	ds_write_b64 v131, v[20:21] offset:720
	s_waitcnt vmcnt(37)
	v_med3_i32 v24, v24, 0, 1
	v_med3_i32 v25, v25, 0, 1
	v_med3_i32 v26, v26, 0, 1
	v_med3_i32 v27, v27, 0, 1
	v_lshl_or_b32 v24, v25, 16, v24
	v_lshl_or_b32 v25, v27, 16, v26
	v_mul_u32_u24_e32 v24, 0xffff, v24
	v_mul_u32_u24_e32 v25, 0xffff, v25
	ds_write_b64 v131, v[24:25] offset:864
	s_waitcnt vmcnt(36)
	v_med3_i32 v28, v28, 0, 1
	v_med3_i32 v29, v29, 0, 1
	v_med3_i32 v30, v30, 0, 1
	v_med3_i32 v31, v31, 0, 1
	v_lshl_or_b32 v28, v29, 16, v28
	v_lshl_or_b32 v29, v31, 16, v30
	v_mul_u32_u24_e32 v28, 0xffff, v28
	v_mul_u32_u24_e32 v29, 0xffff, v29
	ds_write_b64 v131, v[28:29] offset:1008
	s_waitcnt vmcnt(15)
	s_cmp_lg_u32 s8, 0
	s_cbranch_scc1 .Lld_bbs14
	ds_write_b128 v138, v[156:159] offset:18432
.Lld_bbs14:
	s_waitcnt lgkmcnt(0)
	global_load_dwordx4 v[16:19], v132, s[72:73] nt
	global_load_dwordx4 v[20:23], v132, s[74:75] nt
	global_load_dwordx4 v[24:27], v132, s[76:77] nt
	global_load_dwordx4 v[28:31], v132, s[78:79] nt
	global_load_dwordx4 v[152:155], v138, s[14:15]
	s_add_u32 s14, s14, 0x400
	s_addc_u32 s15, s15, 0
	s_add_i32 s16, s16, 1
	s_cmp_lg_u32 s16, 48
	s_cbranch_scc1 .Lld_bbn18
	s_mov_b32 s16, 0
	s_add_i32 s17, s17, 1
	s_cmp_lg_u32 s17, 48
	s_cbranch_scc1 .Lld_bbw18
	s_mov_b32 s17, 0
	s_branch .Lld_bbn18

.Lld_nf13:
	s_add_i32 s9, s9, 1
	s_cmp_eq_u32 s9, 48
	s_cselect_b32 s9, 0, s9
	s_waitcnt vmcnt(39)
	v_med3_i32 v32, v32, 0, 1
	v_med3_i32 v33, v33, 0, 1
	v_med3_i32 v34, v34, 0, 1
	v_med3_i32 v35, v35, 0, 1
	v_lshl_or_b32 v32, v33, 16, v32
	v_lshl_or_b32 v33, v35, 16, v34
	v_mul_u32_u24_e32 v32, 0xffff, v32
	v_mul_u32_u24_e32 v33, 0xffff, v33
	ds_write_b64 v131, v[32:33] offset:1152
	s_waitcnt vmcnt(38)
	v_med3_i32 v36, v36, 0, 1
	v_med3_i32 v37, v37, 0, 1
	v_med3_i32 v38, v38, 0, 1
	v_med3_i32 v39, v39, 0, 1
	v_lshl_or_b32 v36, v37, 16, v36
	v_lshl_or_b32 v37, v39, 16, v38
	v_mul_u32_u24_e32 v36, 0xffff, v36
	v_mul_u32_u24_e32 v37, 0xffff, v37
	ds_write_b64 v131, v[36:37] offset:1296
	s_waitcnt vmcnt(37)
	v_med3_i32 v40, v40, 0, 1
	v_med3_i32 v41, v41, 0, 1
	v_med3_i32 v42, v42, 0, 1
	v_med3_i32 v43, v43, 0, 1
	v_lshl_or_b32 v40, v41, 16, v40
	v_lshl_or_b32 v41, v43, 16, v42
	v_mul_u32_u24_e32 v40, 0xffff, v40
	v_mul_u32_u24_e32 v41, 0xffff, v41
	ds_write_b64 v131, v[40:41] offset:1440
	s_waitcnt vmcnt(36)
	v_med3_i32 v44, v44, 0, 1
	v_med3_i32 v45, v45, 0, 1
	v_med3_i32 v46, v46, 0, 1
	v_med3_i32 v47, v47, 0, 1
	v_lshl_or_b32 v44, v45, 16, v44
	v_lshl_or_b32 v45, v47, 16, v46
	v_mul_u32_u24_e32 v44, 0xffff, v44
	v_mul_u32_u24_e32 v45, 0xffff, v45
	ds_write_b64 v131, v[44:45] offset:1584
	s_waitcnt vmcnt(15)
	s_cmp_lg_u32 s8, 0
	s_cbranch_scc1 .Lld_bbs15
	ds_write_b128 v138, v[140:143] offset:19456
.Lld_bbs15:
	s_waitcnt lgkmcnt(0)
	global_load_dwordx4 v[32:35], v132, s[80:81] nt
	global_load_dwordx4 v[36:39], v132, s[82:83] nt
	global_load_dwordx4 v[40:43], v132, s[84:85] nt
	global_load_dwordx4 v[44:47], v132, s[86:87] nt
	global_load_dwordx4 v[156:159], v138, s[14:15]
	s_add_u32 s14, s14, 0x400
	s_addc_u32 s15, s15, 0
	s_add_i32 s16, s16, 1
	s_cmp_lg_u32 s16, 48
	s_cbranch_scc1 .Lld_bbn19
	s_mov_b32 s16, 0
	s_add_i32 s17, s17, 1
	s_cmp_lg_u32 s17, 48
	s_cbranch_scc1 .Lld_bbw19
	s_mov_b32 s17, 0
	s_branch .Lld_bbn19

.Lld_nf14:
	s_add_i32 s9, s9, 1
	s_cmp_eq_u32 s9, 48
	s_cselect_b32 s9, 0, s9
	s_waitcnt vmcnt(39)
	v_med3_i32 v48, v48, 0, 1
	v_med3_i32 v49, v49, 0, 1
	v_med3_i32 v50, v50, 0, 1
	v_med3_i32 v51, v51, 0, 1
	v_lshl_or_b32 v48, v49, 16, v48
	v_lshl_or_b32 v49, v51, 16, v50
	v_mul_u32_u24_e32 v48, 0xffff, v48
	v_mul_u32_u24_e32 v49, 0xffff, v49
	ds_write_b64 v131, v[48:49] offset:1728
	s_waitcnt vmcnt(38)
	v_med3_i32 v52, v52, 0, 1
	v_med3_i32 v53, v53, 0, 1
	v_med3_i32 v54, v54, 0, 1
	v_med3_i32 v55, v55, 0, 1
	v_lshl_or_b32 v52, v53, 16, v52
	v_lshl_or_b32 v53, v55, 16, v54
	v_mul_u32_u24_e32 v52, 0xffff, v52
	v_mul_u32_u24_e32 v53, 0xffff, v53
	ds_write_b64 v131, v[52:53] offset:1872
	s_waitcnt vmcnt(37)
	v_med3_i32 v56, v56, 0, 1
	v_med3_i32 v57, v57, 0, 1
	v_med3_i32 v58, v58, 0, 1
	v_med3_i32 v59, v59, 0, 1
	v_lshl_or_b32 v56, v57, 16, v56
	v_lshl_or_b32 v57, v59, 16, v58
	v_mul_u32_u24_e32 v56, 0xffff, v56
	v_mul_u32_u24_e32 v57, 0xffff, v57
	ds_write_b64 v131, v[56:57] offset:2016
	s_waitcnt vmcnt(36)
	v_med3_i32 v60, v60, 0, 1
	v_med3_i32 v61, v61, 0, 1
	v_med3_i32 v62, v62, 0, 1
	v_med3_i32 v63, v63, 0, 1
	v_lshl_or_b32 v60, v61, 16, v60
	v_lshl_or_b32 v61, v63, 16, v62
	v_mul_u32_u24_e32 v60, 0xffff, v60
	v_mul_u32_u24_e32 v61, 0xffff, v61
	ds_write_b64 v131, v[60:61] offset:2160
	s_waitcnt vmcnt(15)
	s_cmp_lg_u32 s8, 0
	s_cbranch_scc1 .Lld_bbs16
	ds_write_b128 v138, v[144:147] offset:18432
.Lld_bbs16:
	s_waitcnt lgkmcnt(0)
	global_load_dwordx4 v[48:51], v132, s[88:89] nt
	global_load_dwordx4 v[52:55], v132, s[90:91] nt
	global_load_dwordx4 v[56:59], v132, s[92:93] nt
	global_load_dwordx4 v[60:63], v132, s[94:95] nt
	global_load_dwordx4 v[140:143], v138, s[14:15]
	s_add_u32 s14, s14, 0x400
	s_addc_u32 s15, s15, 0
	s_add_i32 s16, s16, 1
	s_cmp_lg_u32 s16, 48
	s_cbranch_scc1 .Lld_bbn20
	s_mov_b32 s16, 0
	s_add_i32 s17, s17, 1
	s_cmp_lg_u32 s17, 48
	s_cbranch_scc1 .Lld_bbw20
	s_mov_b32 s17, 0
	s_branch .Lld_bbn20

.Lld_nf15:
	s_add_i32 s9, s9, 1
	s_cmp_eq_u32 s9, 48
	s_cselect_b32 s9, 0, s9
	s_waitcnt vmcnt(39)
	v_med3_i32 v64, v64, 0, 1
	v_med3_i32 v65, v65, 0, 1
	v_med3_i32 v66, v66, 0, 1
	v_med3_i32 v67, v67, 0, 1
	v_lshl_or_b32 v64, v65, 16, v64
	v_lshl_or_b32 v65, v67, 16, v66
	v_mul_u32_u24_e32 v64, 0xffff, v64
	v_mul_u32_u24_e32 v65, 0xffff, v65
	ds_write_b64 v131, v[64:65] offset:36864
	s_waitcnt vmcnt(38)
	v_med3_i32 v68, v68, 0, 1
	v_med3_i32 v69, v69, 0, 1
	v_med3_i32 v70, v70, 0, 1
	v_med3_i32 v71, v71, 0, 1
	v_lshl_or_b32 v68, v69, 16, v68
	v_lshl_or_b32 v69, v71, 16, v70
	v_mul_u32_u24_e32 v68, 0xffff, v68
	v_mul_u32_u24_e32 v69, 0xffff, v69
	ds_write_b64 v131, v[68:69] offset:37008
	s_waitcnt vmcnt(37)
	v_med3_i32 v72, v72, 0, 1
	v_med3_i32 v73, v73, 0, 1
	v_med3_i32 v74, v74, 0, 1
	v_med3_i32 v75, v75, 0, 1
	v_lshl_or_b32 v72, v73, 16, v72
	v_lshl_or_b32 v73, v75, 16, v74
	v_mul_u32_u24_e32 v72, 0xffff, v72
	v_mul_u32_u24_e32 v73, 0xffff, v73
	ds_write_b64 v131, v[72:73] offset:37152
	s_waitcnt vmcnt(36)
	v_med3_i32 v76, v76, 0, 1
	v_med3_i32 v77, v77, 0, 1
	v_med3_i32 v78, v78, 0, 1
	v_med3_i32 v79, v79, 0, 1
	v_lshl_or_b32 v76, v77, 16, v76
	v_lshl_or_b32 v77, v79, 16, v78
	v_mul_u32_u24_e32 v76, 0xffff, v76
	v_mul_u32_u24_e32 v77, 0xffff, v77
	ds_write_b64 v131, v[76:77] offset:37296
	s_waitcnt vmcnt(15)
	s_cmp_lg_u32 s8, 0
	s_cbranch_scc1 .Lld_bbs17
	ds_write_b128 v138, v[148:151] offset:19456
.Lld_bbs17:
	s_waitcnt lgkmcnt(0)
	global_load_dwordx4 v[144:147], v138, s[14:15]
	s_add_u32 s14, s14, 0x400
	s_addc_u32 s15, s15, 0
	s_add_i32 s16, s16, 1
	s_cmp_lg_u32 s16, 48
	s_cbranch_scc1 .Lld_bbn21
	s_mov_b32 s16, 0
	s_add_i32 s17, s17, 1
	s_cmp_lg_u32 s17, 48
	s_cbranch_scc1 .Lld_bbw21
	s_mov_b32 s17, 0
	s_branch .Lld_bbn21

.Lld_nf16:
	s_add_i32 s9, s9, 1
	s_cmp_eq_u32 s9, 48
	s_cselect_b32 s9, 0, s9
	s_waitcnt vmcnt(35)
	v_med3_i32 v80, v80, 0, 1
	v_med3_i32 v81, v81, 0, 1
	v_med3_i32 v82, v82, 0, 1
	v_med3_i32 v83, v83, 0, 1
	v_lshl_or_b32 v80, v81, 16, v80
	v_lshl_or_b32 v81, v83, 16, v82
	v_mul_u32_u24_e32 v80, 0xffff, v80
	v_mul_u32_u24_e32 v81, 0xffff, v81
	ds_write_b64 v131, v[80:81] offset:37440
	s_waitcnt vmcnt(34)
	v_med3_i32 v84, v84, 0, 1
	v_med3_i32 v85, v85, 0, 1
	v_med3_i32 v86, v86, 0, 1
	v_med3_i32 v87, v87, 0, 1
	v_lshl_or_b32 v84, v85, 16, v84
	v_lshl_or_b32 v85, v87, 16, v86
	v_mul_u32_u24_e32 v84, 0xffff, v84
	v_mul_u32_u24_e32 v85, 0xffff, v85
	ds_write_b64 v131, v[84:85] offset:37584
	s_waitcnt vmcnt(33)
	v_med3_i32 v88, v88, 0, 1
	v_med3_i32 v89, v89, 0, 1
	v_med3_i32 v90, v90, 0, 1
	v_med3_i32 v91, v91, 0, 1
	v_lshl_or_b32 v88, v89, 16, v88
	v_lshl_or_b32 v89, v91, 16, v90
	v_mul_u32_u24_e32 v88, 0xffff, v88
	v_mul_u32_u24_e32 v89, 0xffff, v89
	ds_write_b64 v131, v[88:89] offset:37728
	s_waitcnt vmcnt(32)
	v_med3_i32 v92, v92, 0, 1
	v_med3_i32 v93, v93, 0, 1
	v_med3_i32 v94, v94, 0, 1
	v_med3_i32 v95, v95, 0, 1
	v_lshl_or_b32 v92, v93, 16, v92
	v_lshl_or_b32 v93, v95, 16, v94
	v_mul_u32_u24_e32 v92, 0xffff, v92
	v_mul_u32_u24_e32 v93, 0xffff, v93
	ds_write_b64 v131, v[92:93] offset:37872
	s_waitcnt vmcnt(11)
	s_cmp_lg_u32 s8, 0
	s_cbranch_scc1 .Lld_bbs18
	ds_write_b128 v138, v[152:155] offset:18432
.Lld_bbs18:
	s_waitcnt lgkmcnt(0)
	global_load_dwordx4 v[148:151], v138, s[14:15]
	s_add_u32 s14, s14, 0x400
	s_addc_u32 s15, s15, 0
	s_add_i32 s16, s16, 1
	s_cmp_lg_u32 s16, 48
	s_cbranch_scc1 .Lld_bbn22
	s_mov_b32 s16, 0
	s_add_i32 s17, s17, 1
	s_cmp_lg_u32 s17, 48
	s_cbranch_scc1 .Lld_bbw22
	s_mov_b32 s17, 0
	s_branch .Lld_bbn22

.Lld_nf17:
	s_add_i32 s9, s9, 1
	s_cmp_eq_u32 s9, 48
	s_cselect_b32 s9, 0, s9
	s_waitcnt vmcnt(31)
	v_med3_i32 v96, v96, 0, 1
	v_med3_i32 v97, v97, 0, 1
	v_med3_i32 v98, v98, 0, 1
	v_med3_i32 v99, v99, 0, 1
	v_lshl_or_b32 v96, v97, 16, v96
	v_lshl_or_b32 v97, v99, 16, v98
	v_mul_u32_u24_e32 v96, 0xffff, v96
	v_mul_u32_u24_e32 v97, 0xffff, v97
	ds_write_b64 v131, v[96:97] offset:38016
	s_waitcnt vmcnt(30)
	v_med3_i32 v100, v100, 0, 1
	v_med3_i32 v101, v101, 0, 1
	v_med3_i32 v102, v102, 0, 1
	v_med3_i32 v103, v103, 0, 1
	v_lshl_or_b32 v100, v101, 16, v100
	v_lshl_or_b32 v101, v103, 16, v102
	v_mul_u32_u24_e32 v100, 0xffff, v100
	v_mul_u32_u24_e32 v101, 0xffff, v101
	ds_write_b64 v131, v[100:101] offset:38160
	s_waitcnt vmcnt(29)
	v_med3_i32 v104, v104, 0, 1
	v_med3_i32 v105, v105, 0, 1
	v_med3_i32 v106, v106, 0, 1
	v_med3_i32 v107, v107, 0, 1
	v_lshl_or_b32 v104, v105, 16, v104
	v_lshl_or_b32 v105, v107, 16, v106
	v_mul_u32_u24_e32 v104, 0xffff, v104
	v_mul_u32_u24_e32 v105, 0xffff, v105
	ds_write_b64 v131, v[104:105] offset:38304
	s_waitcnt vmcnt(28)
	v_med3_i32 v108, v108, 0, 1
	v_med3_i32 v109, v109, 0, 1
	v_med3_i32 v110, v110, 0, 1
	v_med3_i32 v111, v111, 0, 1
	v_lshl_or_b32 v108, v109, 16, v108
	v_lshl_or_b32 v109, v111, 16, v110
	v_mul_u32_u24_e32 v108, 0xffff, v108
	v_mul_u32_u24_e32 v109, 0xffff, v109
	ds_write_b64 v131, v[108:109] offset:38448
	s_waitcnt vmcnt(7)
	s_cmp_lg_u32 s8, 0
	s_cbranch_scc1 .Lld_bbs19
	ds_write_b128 v138, v[156:159] offset:19456
.Lld_bbs19:
	s_waitcnt lgkmcnt(0)
	global_load_dwordx4 v[152:155], v138, s[14:15]
	s_add_u32 s14, s14, 0x400
	s_addc_u32 s15, s15, 0
	s_add_i32 s16, s16, 1
	s_cmp_lg_u32 s16, 48
	s_cbranch_scc1 .Lld_bbn23
	s_mov_b32 s16, 0
	s_add_i32 s17, s17, 1
	s_cmp_lg_u32 s17, 48
	s_cbranch_scc1 .Lld_bbw23
	s_mov_b32 s17, 0
	s_branch .Lld_bbn23

.Lld_nf18:
	s_add_i32 s9, s9, 1
	s_cmp_eq_u32 s9, 48
	s_cselect_b32 s9, 0, s9
	s_waitcnt vmcnt(27)
	v_med3_i32 v112, v112, 0, 1
	v_med3_i32 v113, v113, 0, 1
	v_med3_i32 v114, v114, 0, 1
	v_med3_i32 v115, v115, 0, 1
	v_lshl_or_b32 v112, v113, 16, v112
	v_lshl_or_b32 v113, v115, 16, v114
	v_mul_u32_u24_e32 v112, 0xffff, v112
	v_mul_u32_u24_e32 v113, 0xffff, v113
	ds_write_b64 v131, v[112:113] offset:38592
	s_waitcnt vmcnt(26)
	v_med3_i32 v116, v116, 0, 1
	v_med3_i32 v117, v117, 0, 1
	v_med3_i32 v118, v118, 0, 1
	v_med3_i32 v119, v119, 0, 1
	v_lshl_or_b32 v116, v117, 16, v116
	v_lshl_or_b32 v117, v119, 16, v118
	v_mul_u32_u24_e32 v116, 0xffff, v116
	v_mul_u32_u24_e32 v117, 0xffff, v117
	ds_write_b64 v131, v[116:117] offset:38736
	s_waitcnt vmcnt(25)
	v_med3_i32 v120, v120, 0, 1
	v_med3_i32 v121, v121, 0, 1
	v_med3_i32 v122, v122, 0, 1
	v_med3_i32 v123, v123, 0, 1
	v_lshl_or_b32 v120, v121, 16, v120
	v_lshl_or_b32 v121, v123, 16, v122
	v_mul_u32_u24_e32 v120, 0xffff, v120
	v_mul_u32_u24_e32 v121, 0xffff, v121
	ds_write_b64 v131, v[120:121] offset:38880
	s_waitcnt vmcnt(24)
	v_med3_i32 v124, v124, 0, 1
	v_med3_i32 v125, v125, 0, 1
	v_med3_i32 v126, v126, 0, 1
	v_med3_i32 v127, v127, 0, 1
	v_lshl_or_b32 v124, v125, 16, v124
	v_lshl_or_b32 v125, v127, 16, v126
	v_mul_u32_u24_e32 v124, 0xffff, v124
	v_mul_u32_u24_e32 v125, 0xffff, v125
	ds_write_b64 v131, v[124:125] offset:39024
	s_waitcnt vmcnt(3)
	s_cmp_lg_u32 s8, 0
	s_cbranch_scc1 .Lld_bbs20
	ds_write_b128 v138, v[140:143] offset:18432
.Lld_bbs20:
	s_waitcnt lgkmcnt(0)
	global_load_dwordx4 v[156:159], v138, s[14:15]
	s_add_u32 s14, s14, 0x400
	s_addc_u32 s15, s15, 0
	s_add_i32 s16, s16, 1
	s_cmp_lg_u32 s16, 48
	s_cbranch_scc1 .Lld_bbn24
	s_mov_b32 s16, 0
	s_add_i32 s17, s17, 1
	s_cmp_lg_u32 s17, 48
	s_cbranch_scc1 .Lld_bbw24
	s_mov_b32 s17, 0
	s_branch .Lld_bbn24

.Lld_nf19:
	s_add_i32 s9, s9, 1
	s_cmp_eq_u32 s9, 48
	s_cselect_b32 s9, 0, s9
	s_waitcnt vmcnt(23)
	v_med3_i32 v0, v0, 0, 1
	v_med3_i32 v1, v1, 0, 1
	v_med3_i32 v2, v2, 0, 1
	v_med3_i32 v3, v3, 0, 1
	v_lshl_or_b32 v0, v1, 16, v0
	v_lshl_or_b32 v1, v3, 16, v2
	v_mul_u32_u24_e32 v0, 0xffff, v0
	v_mul_u32_u24_e32 v1, 0xffff, v1
	ds_write_b64 v131, v[0:1] offset:0
	s_waitcnt vmcnt(22)
	v_med3_i32 v4, v4, 0, 1
	v_med3_i32 v5, v5, 0, 1
	v_med3_i32 v6, v6, 0, 1
	v_med3_i32 v7, v7, 0, 1
	v_lshl_or_b32 v4, v5, 16, v4
	v_lshl_or_b32 v5, v7, 16, v6
	v_mul_u32_u24_e32 v4, 0xffff, v4
	v_mul_u32_u24_e32 v5, 0xffff, v5
	ds_write_b64 v131, v[4:5] offset:144
	s_waitcnt vmcnt(21)
	v_med3_i32 v8, v8, 0, 1
	v_med3_i32 v9, v9, 0, 1
	v_med3_i32 v10, v10, 0, 1
	v_med3_i32 v11, v11, 0, 1
	v_lshl_or_b32 v8, v9, 16, v8
	v_lshl_or_b32 v9, v11, 16, v10
	v_mul_u32_u24_e32 v8, 0xffff, v8
	v_mul_u32_u24_e32 v9, 0xffff, v9
	ds_write_b64 v131, v[8:9] offset:288
	s_waitcnt vmcnt(20)
	v_med3_i32 v12, v12, 0, 1
	v_med3_i32 v13, v13, 0, 1
	v_med3_i32 v14, v14, 0, 1
	v_med3_i32 v15, v15, 0, 1
	v_lshl_or_b32 v12, v13, 16, v12
	v_lshl_or_b32 v13, v15, 16, v14
	v_mul_u32_u24_e32 v12, 0xffff, v12
	v_mul_u32_u24_e32 v13, 0xffff, v13
	ds_write_b64 v131, v[12:13] offset:432
	s_waitcnt vmcnt(3)
	s_cmp_lg_u32 s8, 0
	s_cbranch_scc1 .Lld_bbs21
	ds_write_b128 v138, v[144:147] offset:19456
.Lld_bbs21:
	s_waitcnt lgkmcnt(0)
	global_load_dwordx4 v[140:143], v138, s[14:15]
	s_add_u32 s14, s14, 0x400
	s_addc_u32 s15, s15, 0
	s_add_i32 s16, s16, 1
	s_cmp_lg_u32 s16, 48
	s_cbranch_scc1 .Lld_bbn25
	s_mov_b32 s16, 0
	s_add_i32 s17, s17, 1
	s_cmp_lg_u32 s17, 48
	s_cbranch_scc1 .Lld_bbw25
	s_mov_b32 s17, 0
	s_branch .Lld_bbn25

.Lld_nf20:
	s_add_i32 s9, s9, 1
	s_cmp_eq_u32 s9, 48
	s_cselect_b32 s9, 0, s9
	s_waitcnt vmcnt(19)
	v_med3_i32 v16, v16, 0, 1
	v_med3_i32 v17, v17, 0, 1
	v_med3_i32 v18, v18, 0, 1
	v_med3_i32 v19, v19, 0, 1
	v_lshl_or_b32 v16, v17, 16, v16
	v_lshl_or_b32 v17, v19, 16, v18
	v_mul_u32_u24_e32 v16, 0xffff, v16
	v_mul_u32_u24_e32 v17, 0xffff, v17
	ds_write_b64 v131, v[16:17] offset:576
	s_waitcnt vmcnt(18)
	v_med3_i32 v20, v20, 0, 1
	v_med3_i32 v21, v21, 0, 1
	v_med3_i32 v22, v22, 0, 1
	v_med3_i32 v23, v23, 0, 1
	v_lshl_or_b32 v20, v21, 16, v20
	v_lshl_or_b32 v21, v23, 16, v22
	v_mul_u32_u24_e32 v20, 0xffff, v20
	v_mul_u32_u24_e32 v21, 0xffff, v21
	ds_write_b64 v131, v[20:21] offset:720
	s_waitcnt vmcnt(17)
	v_med3_i32 v24, v24, 0, 1
	v_med3_i32 v25, v25, 0, 1
	v_med3_i32 v26, v26, 0, 1
	v_med3_i32 v27, v27, 0, 1
	v_lshl_or_b32 v24, v25, 16, v24
	v_lshl_or_b32 v25, v27, 16, v26
	v_mul_u32_u24_e32 v24, 0xffff, v24
	v_mul_u32_u24_e32 v25, 0xffff, v25
	ds_write_b64 v131, v[24:25] offset:864
	s_waitcnt vmcnt(16)
	v_med3_i32 v28, v28, 0, 1
	v_med3_i32 v29, v29, 0, 1
	v_med3_i32 v30, v30, 0, 1
	v_med3_i32 v31, v31, 0, 1
	v_lshl_or_b32 v28, v29, 16, v28
	v_lshl_or_b32 v29, v31, 16, v30
	v_mul_u32_u24_e32 v28, 0xffff, v28
	v_mul_u32_u24_e32 v29, 0xffff, v29
	ds_write_b64 v131, v[28:29] offset:1008
	s_waitcnt vmcnt(3)
	s_cmp_lg_u32 s8, 0
	s_cbranch_scc1 .Lld_bbs22
	ds_write_b128 v138, v[148:151] offset:18432

.Lld_nf21:
	s_add_i32 s9, s9, 1
	s_cmp_eq_u32 s9, 48
	s_cselect_b32 s9, 0, s9
	s_waitcnt vmcnt(15)
	v_med3_i32 v32, v32, 0, 1
	v_med3_i32 v33, v33, 0, 1
	v_med3_i32 v34, v34, 0, 1
	v_med3_i32 v35, v35, 0, 1
	v_lshl_or_b32 v32, v33, 16, v32
	v_lshl_or_b32 v33, v35, 16, v34
	v_mul_u32_u24_e32 v32, 0xffff, v32
	v_mul_u32_u24_e32 v33, 0xffff, v33
	ds_write_b64 v131, v[32:33] offset:1152
	s_waitcnt vmcnt(14)
	v_med3_i32 v36, v36, 0, 1
	v_med3_i32 v37, v37, 0, 1
	v_med3_i32 v38, v38, 0, 1
	v_med3_i32 v39, v39, 0, 1
	v_lshl_or_b32 v36, v37, 16, v36
	v_lshl_or_b32 v37, v39, 16, v38
	v_mul_u32_u24_e32 v36, 0xffff, v36
	v_mul_u32_u24_e32 v37, 0xffff, v37
	ds_write_b64 v131, v[36:37] offset:1296
	s_waitcnt vmcnt(13)
	v_med3_i32 v40, v40, 0, 1
	v_med3_i32 v41, v41, 0, 1
	v_med3_i32 v42, v42, 0, 1
	v_med3_i32 v43, v43, 0, 1
	v_lshl_or_b32 v40, v41, 16, v40
	v_lshl_or_b32 v41, v43, 16, v42
	v_mul_u32_u24_e32 v40, 0xffff, v40
	v_mul_u32_u24_e32 v41, 0xffff, v41
	ds_write_b64 v131, v[40:41] offset:1440
	s_waitcnt vmcnt(12)
	v_med3_i32 v44, v44, 0, 1
	v_med3_i32 v45, v45, 0, 1
	v_med3_i32 v46, v46, 0, 1
	v_med3_i32 v47, v47, 0, 1
	v_lshl_or_b32 v44, v45, 16, v44
	v_lshl_or_b32 v45, v47, 16, v46
	v_mul_u32_u24_e32 v44, 0xffff, v44
	v_mul_u32_u24_e32 v45, 0xffff, v45
	ds_write_b64 v131, v[44:45] offset:1584
	s_waitcnt vmcnt(3)
	s_cmp_lg_u32 s8, 0
	s_cbranch_scc1 .Lld_bbs23
	ds_write_b128 v138, v[152:155] offset:19456
.Lld_bbs23:
	s_waitcnt lgkmcnt(0)
	s_barrier
	s_cmp_lg_u32 s9, 47
	s_cbranch_scc1 .Lld_nf22
	s_barrier
.Lld_nf22:
	s_add_i32 s9, s9, 1
	s_cmp_eq_u32 s9, 48
	s_cselect_b32 s9, 0, s9
	s_waitcnt vmcnt(10)
	v_med3_i32 v48, v48, 0, 1
	v_med3_i32 v49, v49, 0, 1
	v_med3_i32 v50, v50, 0, 1
	v_med3_i32 v51, v51, 0, 1
	v_lshl_or_b32 v48, v49, 16, v48
	v_lshl_or_b32 v49, v51, 16, v50
	v_mul_u32_u24_e32 v48, 0xffff, v48
	v_mul_u32_u24_e32 v49, 0xffff, v49
	ds_write_b64 v131, v[48:49] offset:1728
	s_waitcnt vmcnt(9)
	v_med3_i32 v52, v52, 0, 1
	v_med3_i32 v53, v53, 0, 1
	v_med3_i32 v54, v54, 0, 1
	v_med3_i32 v55, v55, 0, 1
	v_lshl_or_b32 v52, v53, 16, v52
	v_lshl_or_b32 v53, v55, 16, v54
	v_mul_u32_u24_e32 v52, 0xffff, v52
	v_mul_u32_u24_e32 v53, 0xffff, v53
	ds_write_b64 v131, v[52:53] offset:1872
	s_waitcnt vmcnt(8)
	v_med3_i32 v56, v56, 0, 1
	v_med3_i32 v57, v57, 0, 1
	v_med3_i32 v58, v58, 0, 1
	v_med3_i32 v59, v59, 0, 1
	v_lshl_or_b32 v56, v57, 16, v56
	v_lshl_or_b32 v57, v59, 16, v58
	v_mul_u32_u24_e32 v56, 0xffff, v56
	v_mul_u32_u24_e32 v57, 0xffff, v57
	ds_write_b64 v131, v[56:57] offset:2016
	s_waitcnt vmcnt(7)
	v_med3_i32 v60, v60, 0, 1
	v_med3_i32 v61, v61, 0, 1
	v_med3_i32 v62, v62, 0, 1
	v_med3_i32 v63, v63, 0, 1
	v_lshl_or_b32 v60, v61, 16, v60
	v_lshl_or_b32 v61, v63, 16, v62
	v_mul_u32_u24_e32 v60, 0xffff, v60
	v_mul_u32_u24_e32 v61, 0xffff, v61
	ds_write_b64 v131, v[60:61] offset:2160
	s_waitcnt vmcnt(2)
	s_cmp_lg_u32 s8, 0
	s_cbranch_scc1 .Lld_bbs24
	ds_write_b128 v138, v[156:159] offset:18432

.Lld_nf23:
	s_add_i32 s9, s9, 1
	s_cmp_eq_u32 s9, 48
	s_cselect_b32 s9, 0, s9
	s_waitcnt vmcnt(1)
	s_cmp_lg_u32 s8, 0
	s_cbranch_scc1 .Lld_bbs25
	ds_write_b128 v138, v[140:143] offset:19456

.Lld_nf24:
	s_add_i32 s9, s9, 1
	s_cmp_eq_u32 s9, 48
	s_cselect_b32 s9, 0, s9
	s_waitcnt vmcnt(0)
	s_cmp_lg_u32 s8, 0
	s_cbranch_scc1 .Lld_bbs26
	ds_write_b128 v138, v[144:147] offset:18432

.Lld_nf25:
	s_add_i32 s9, s9, 1
	s_cmp_eq_u32 s9, 48
	s_cselect_b32 s9, 0, s9
	s_waitcnt lgkmcnt(0)
	s_barrier
	s_barrier

	.amdhsa_kernel _Z11attn_kernelPKiPKDv8_DF16_PKDF16_S5_PDF16_Pf
		.amdhsa_group_segment_fixed_size 160768
		.amdhsa_private_segment_fixed_size 0
		.amdhsa_kernarg_size 48
		.amdhsa_user_sgpr_count 2
		.amdhsa_user_sgpr_dispatch_ptr 0
		.amdhsa_user_sgpr_queue_ptr 0
		.amdhsa_user_sgpr_kernarg_segment_ptr 1
		.amdhsa_user_sgpr_dispatch_id 0
		.amdhsa_user_sgpr_kernarg_preload_length 0
		.amdhsa_user_sgpr_kernarg_preload_offset 0
		.amdhsa_user_sgpr_private_segment_size 0
		.amdhsa_uses_dynamic_stack 0
		.amdhsa_enable_private_segment 0
		.amdhsa_system_sgpr_workgroup_id_x 1
		.amdhsa_system_sgpr_workgroup_id_y 0
		.amdhsa_system_sgpr_workgroup_id_z 0
		.amdhsa_system_sgpr_workgroup_info 0
		.amdhsa_system_vgpr_workitem_id 0
		.amdhsa_next_free_vgpr 168
		.amdhsa_next_free_sgpr 96
		.amdhsa_accum_offset 168
		.amdhsa_reserve_vcc 1
		.amdhsa_float_round_mode_32 0
		.amdhsa_float_round_mode_16_64 0
		.amdhsa_float_denorm_mode_32 3
		.amdhsa_float_denorm_mode_16_64 3
		.amdhsa_dx10_clamp 1
		.amdhsa_ieee_mode 1
		.amdhsa_fp16_overflow 0
		.amdhsa_tg_split 0
		.amdhsa_exception_fp_ieee_invalid_op 0
		.amdhsa_exception_fp_denorm_src 0
		.amdhsa_exception_fp_ieee_div_zero 0
		.amdhsa_exception_fp_ieee_overflow 0
		.amdhsa_exception_fp_ieee_underflow 0
		.amdhsa_exception_fp_ieee_inexact 0
		.amdhsa_exception_int_div_zero 0
	.end_amdhsa_kernel

amdhsa.kernels:
  - .agpr_count:     0
    .args:
      - .actual_access:  read_only
        .address_space:  global
        .offset:         0
        .size:           8
        .value_kind:     global_buffer
      - .actual_access:  read_only
        .address_space:  global
        .offset:         8
        .size:           8
        .value_kind:     global_buffer
      - .actual_access:  read_only
        .address_space:  global
        .offset:         16
        .size:           8
        .value_kind:     global_buffer
      - .actual_access:  write_only
        .address_space:  global
        .offset:         24
        .size:           8
        .value_kind:     global_buffer
      - .actual_access:  write_only
        .address_space:  global
        .offset:         32
        .size:           8
        .value_kind:     global_buffer
      - .actual_access:  write_only
        .address_space:  global
        .offset:         40
        .size:           8
        .value_kind:     global_buffer
    .group_segment_fixed_size: 57344
    .kernarg_segment_align: 8
    .kernarg_segment_size: 48
    .language:       OpenCL C
    .language_version:
      - 2
      - 0
    .max_flat_workgroup_size: 512
    .name:           _Z12gemm1_kernelPKfS0_S0_PDv8_DF16_PDF16_S3_
    .private_segment_fixed_size: 0
    .sgpr_count:     18
    .sgpr_spill_count: 0
    .symbol:         _Z12gemm1_kernelPKfS0_S0_PDv8_DF16_PDF16_S3_.kd
    .uniform_work_group_size: 1
    .uses_dynamic_stack: false
    .vgpr_count:     125
    .vgpr_spill_count: 0
    .wavefront_size: 64
  - .agpr_count:     0
    .args:
      - .actual_access:  read_only
        .address_space:  global
        .offset:         0
        .size:           8
        .value_kind:     global_buffer
      - .actual_access:  read_only
        .address_space:  global
        .offset:         8
        .size:           8
        .value_kind:     global_buffer
      - .actual_access:  read_only
        .address_space:  global
        .offset:         16
        .size:           8
        .value_kind:     global_buffer
      - .actual_access:  read_only
        .address_space:  global
        .offset:         24
        .size:           8
        .value_kind:     global_buffer
      - .actual_access:  write_only
        .address_space:  global
        .offset:         32
        .size:           8
        .value_kind:     global_buffer
      - .actual_access:  write_only
        .address_space:  global
        .offset:         40
        .size:           8
        .value_kind:     global_buffer
    .group_segment_fixed_size: 160768
    .kernarg_segment_align: 8
    .kernarg_segment_size: 48
    .language:       OpenCL C
    .language_version:
      - 2
      - 0
    .max_flat_workgroup_size: 768
    .name:           _Z11attn_kernelPKiPKDv8_DF16_PKDF16_S5_PDF16_Pf
    .private_segment_fixed_size: 0
    .sgpr_count:     55
    .sgpr_spill_count: 0
    .symbol:         _Z11attn_kernelPKiPKDv8_DF16_PKDF16_S5_PDF16_Pf.kd
    .uniform_work_group_size: 1
    .uses_dynamic_stack: false
    .vgpr_count:     168
    .vgpr_spill_count: 0
    .wavefront_size: 64
  - .agpr_count:     12
    .args:
      - .actual_access:  read_only
        .address_space:  global
        .offset:         0
        .size:           8
        .value_kind:     global_buffer
      - .actual_access:  read_only
        .address_space:  global
        .offset:         8
        .size:           8
        .value_kind:     global_buffer
      - .actual_access:  read_only
        .address_space:  global
        .offset:         16
        .size:           8
        .value_kind:     global_buffer
      - .actual_access:  read_only
        .address_space:  global
        .offset:         24
        .size:           8
        .value_kind:     global_buffer
      - .actual_access:  read_only
        .address_space:  global
        .offset:         32
        .size:           8
        .value_kind:     global_buffer
      - .actual_access:  read_only
        .address_space:  global
        .offset:         40
        .size:           8
        .value_kind:     global_buffer
      - .actual_access:  write_only
        .address_space:  global
        .offset:         48
        .size:           8
        .value_kind:     global_buffer
    .group_segment_fixed_size: 16192
    .kernarg_segment_align: 8
    .kernarg_segment_size: 56
    .language:       OpenCL C
    .language_version:
      - 2
      - 0
    .max_flat_workgroup_size: 256
    .name:           _Z10epi_kernelPKDF16_PKfS2_S2_S2_S2_Pf
    .private_segment_fixed_size: 0
    .sgpr_count:     24
    .sgpr_spill_count: 0
    .symbol:         _Z10epi_kernelPKDF16_PKfS2_S2_S2_S2_Pf.kd
    .uniform_work_group_size: 1
    .uses_dynamic_stack: false
    .vgpr_count:     124
    .vgpr_spill_count: 0
    .wavefront_size: 64
